# s30
# baseline (speedup 1.0000x reference)
.LBB1_5:
	v_lshlrev_b32_e32 v67, 4, v1
	v_lshrrev_b32_e32 v1, 1, v1
	v_lshrrev_b32_e32 v69, 5, v132
	v_ashrrev_i32_e32 v66, 4, v132
	v_bitop3_b32 v1, v1, v69, 7 bitop3:0x78
	s_add_u32 s22, s24, s2
	v_lshlrev_b32_e32 v68, 7, v66
	v_lshlrev_b32_e32 v1, 4, v1
	v_and_b32_e32 v0, 8, v0
	s_addc_u32 s90, s25, s3
	v_lshl_or_b32 v201, v66, 12, v67
	v_or3_b32 v0, v68, v1, v0
	v_add_u32_e32 v100, 0x10000, v0
	v_cvt_pk_f16_f32 v1, v64, v65
	v_cvt_pk_f16_f32 v0, v62, v63
	v_cvt_pk_f16_f32 v61, v60, v61
	v_cvt_pk_f16_f32 v60, v58, v59
	ds_write2st64_b64 v100, v[0:1], v[60:61] offset1:8
	v_cvt_pk_f16_f32 v1, v56, v57
	v_cvt_pk_f16_f32 v0, v54, v55
	v_cvt_pk_f16_f32 v53, v52, v53
	v_cvt_pk_f16_f32 v52, v50, v51
	ds_write2st64_b64 v100, v[0:1], v[52:53] offset0:16 offset1:24
	v_cvt_pk_f16_f32 v1, v48, v49
	v_cvt_pk_f16_f32 v0, v46, v47
	v_cvt_pk_f16_f32 v45, v44, v45
	v_cvt_pk_f16_f32 v44, v42, v43
	ds_write2st64_b64 v100, v[0:1], v[44:45] offset0:32 offset1:40
	v_cvt_pk_f16_f32 v1, v40, v41
	v_cvt_pk_f16_f32 v0, v38, v39
	v_cvt_pk_f16_f32 v37, v36, v37
	v_cvt_pk_f16_f32 v36, v34, v35
	ds_write2st64_b64 v100, v[0:1], v[36:37] offset0:48 offset1:56
	s_add_u32 s0, s22, 0x200
	s_addc_u32 s1, s90, 0
	s_add_u32 s70, s0, 0x20000
	s_addc_u32 s71, s1, 0
	s_add_u32 s72, s0, 0x40000
	s_addc_u32 s73, s1, 0
	s_add_u32 s92, s0, 0x60000
	s_addc_u32 s93, s1, 0
	s_add_u32 s94, s0, 0x80000
	s_addc_u32 s95, s1, 0
	s_add_u32 s96, s0, 0xa0000
	s_addc_u32 s97, s1, 0
	s_add_u32 s98, s0, 0xc0000
	s_addc_u32 s99, s1, 0
	s_add_u32 s80, s0, 0xe0000
	s_addc_u32 s81, s1, 0
	global_load_dwordx4 v[70:73], v201, s[0:1] nt
	global_load_dwordx4 v[42:45], v201, s[70:71] nt
	global_load_dwordx4 v[46:49], v201, s[72:73] nt
	global_load_dwordx4 v[66:69], v201, s[92:93] nt
	global_load_dwordx4 v[62:65], v201, s[94:95] nt
	global_load_dwordx4 v[58:61], v201, s[96:97] nt
	global_load_dwordx4 v[54:57], v201, s[98:99] nt
	global_load_dwordx4 v[50:53], v201, s[80:81] nt
	s_waitcnt vmcnt(8)
	s_waitcnt lgkmcnt(0)
	s_barrier
	ds_read_b128 v[34:37], v131
	ds_read_b128 v[38:41], v131 offset:2048
	ds_read_b128 v[74:77], v131 offset:4096
	ds_read_b128 v[78:81], v131 offset:6144
	ds_read_b128 v[82:85], v129
	ds_read_b128 v[86:89], v129 offset:2048
	s_add_u32 s70, s22, 0x300
	v_add_u32_e32 v95, 0x8000, v94
	v_lshl_add_u64 v[0:1], s[26:27], 0, v[196:197]
	s_addc_u32 s71, s90, 0
	v_readfirstlane_b32 s0, v95
	s_mov_b32 m0, s0
	v_cvt_pk_f16_f32 v33, v32, v33
	global_load_lds_dwordx4 v[0:1], off
	v_cvt_pk_f16_f32 v32, v30, v31
	ds_write_b64 v100, v[32:33] offset:32768
	s_setprio 1
	s_waitcnt lgkmcnt(1)
	v_mfma_f32_16x16x32_f16 v[90:93], v[82:85], v[34:37], 0
	v_mfma_f32_16x16x32_f16 v[102:105], v[82:85], v[38:41], 0
	v_mfma_f32_16x16x32_f16 v[106:109], v[82:85], v[74:77], 0
	v_mfma_f32_16x16x32_f16 v[82:85], v[82:85], v[78:81], 0
	v_mfma_f32_16x16x32_f16 v[110:113], v[86:89], v[34:37], 0
	v_mfma_f32_16x16x32_f16 v[114:117], v[86:89], v[38:41], 0
	v_mfma_f32_16x16x32_f16 v[118:121], v[86:89], v[74:77], 0
	v_mfma_f32_16x16x32_f16 v[86:89], v[86:89], v[78:81], 0
	s_setprio 0
	ds_read_b128 v[122:125], v129 offset:4096
	ds_read_b128 v[134:137], v129 offset:6144
	v_add_u32_e32 v96, 0xa000, v94
	v_lshl_add_u64 v[98:99], v[0:1], 0, s[58:59]
	v_readfirstlane_b32 s1, v96
	s_mov_b32 m0, s1
	v_cvt_pk_f16_f32 v29, v28, v29
	global_load_lds_dwordx4 v[98:99], off
	v_cvt_pk_f16_f32 v28, v26, v27
	ds_write_b64 v100, v[28:29] offset:36864
	s_add_u32 s70, s22, 0x20300
	s_addc_u32 s71, s90, 0
	s_add_u32 s100, s22, 0x300
	s_addc_u32 s101, s90, 0
	global_load_dwordx4 v[30:33], v201, s[100:101] nt
	s_setprio 1
	s_waitcnt lgkmcnt(1)
	v_mfma_f32_16x16x32_f16 v[138:141], v[122:125], v[34:37], 0
	v_mfma_f32_16x16x32_f16 v[142:145], v[122:125], v[38:41], 0
	v_mfma_f32_16x16x32_f16 v[146:149], v[122:125], v[74:77], 0
	v_mfma_f32_16x16x32_f16 v[122:125], v[122:125], v[78:81], 0
	v_mfma_f32_16x16x32_f16 v[150:153], v[134:137], v[34:37], 0
	v_mfma_f32_16x16x32_f16 v[154:157], v[134:137], v[38:41], 0
	v_mfma_f32_16x16x32_f16 v[158:161], v[134:137], v[74:77], 0
	v_mfma_f32_16x16x32_f16 v[134:137], v[134:137], v[78:81], 0
	s_setprio 0
	ds_read_b128 v[162:165], v129 offset:8192
	ds_read_b128 v[166:169], v129 offset:10240
	v_add_u32_e32 v97, 0xc000, v94
	v_lshl_add_u64 v[98:99], v[0:1], 0, s[60:61]
	v_readfirstlane_b32 s71, v97
	s_mov_b32 m0, s71
	v_cvt_pk_f16_f32 v25, v24, v25
	global_load_lds_dwordx4 v[98:99], off
	v_cvt_pk_f16_f32 v24, v22, v23
	ds_write_b64 v100, v[24:25] offset:40960
	s_add_u32 s72, s22, 0x40300
	s_addc_u32 s73, s90, 0
	s_add_u32 s100, s22, 0x20300
	s_addc_u32 s101, s90, 0
	global_load_dwordx4 v[26:29], v201, s[100:101] nt
	s_setprio 1
	s_waitcnt lgkmcnt(1)
	v_mfma_f32_16x16x32_f16 v[170:173], v[162:165], v[34:37], 0
	v_mfma_f32_16x16x32_f16 v[174:177], v[162:165], v[38:41], 0
	v_mfma_f32_16x16x32_f16 v[178:181], v[162:165], v[74:77], 0
	v_mfma_f32_16x16x32_f16 v[162:165], v[162:165], v[78:81], 0
	v_mfma_f32_16x16x32_f16 v[182:185], v[166:169], v[34:37], 0
	v_mfma_f32_16x16x32_f16 v[186:189], v[166:169], v[38:41], 0
	v_mfma_f32_16x16x32_f16 v[190:193], v[166:169], v[74:77], 0
	v_mfma_f32_16x16x32_f16 v[166:169], v[166:169], v[78:81], 0
	s_setprio 0
	ds_read_b128 v[202:205], v129 offset:12288
	ds_read_b128 v[206:209], v129 offset:14336
	v_add_u32_e32 v98, 0xe000, v94
	v_lshl_add_u64 v[0:1], v[0:1], 0, s[62:63]
	v_readfirstlane_b32 s72, v98
	s_mov_b32 m0, s72
	s_nop 0
	global_load_lds_dwordx4 v[0:1], off
	v_cvt_pk_f16_f32 v1, v20, v21
	v_cvt_pk_f16_f32 v0, v18, v19
	ds_write_b64 v100, v[0:1] offset:45056
	s_add_u32 s80, s22, 0x60300
	s_addc_u32 s81, s90, 0
	s_add_u32 s100, s22, 0x40300
	s_addc_u32 s101, s90, 0
	global_load_dwordx4 v[22:25], v201, s[100:101] nt
	s_setprio 1
	s_waitcnt lgkmcnt(1)
	v_mfma_f32_16x16x32_f16 v[210:213], v[202:205], v[34:37], 0
	v_mfma_f32_16x16x32_f16 v[214:217], v[202:205], v[38:41], 0
	v_mfma_f32_16x16x32_f16 v[218:221], v[202:205], v[74:77], 0
	v_mfma_f32_16x16x32_f16 v[202:205], v[202:205], v[78:81], 0
	v_mfma_f32_16x16x32_f16 v[74:77], v[206:209], v[74:77], 0
	v_mfma_f32_16x16x32_f16 v[78:81], v[206:209], v[78:81], 0
	v_mfma_f32_16x16x32_f16 v[222:225], v[206:209], v[34:37], 0
	v_mfma_f32_16x16x32_f16 v[226:229], v[206:209], v[38:41], 0
	s_setprio 0
	ds_read_b128 v[206:209], v128
	ds_read_b128 v[230:233], v128 offset:2048
	ds_read_b128 v[234:237], v128 offset:4096
	ds_read_b128 v[238:241], v128 offset:6144
	ds_read_b128 v[34:37], v130
	ds_read_b128 v[38:41], v130 offset:2048
	v_cvt_pk_f16_f32 v1, v16, v17
	v_cvt_pk_f16_f32 v0, v14, v15
	ds_write_b64 v100, v[0:1] offset:49152
	s_add_u32 s80, s22, 0x80300
	s_addc_u32 s81, s90, 0
	s_add_u32 s100, s22, 0x60300
	s_addc_u32 s101, s90, 0
	global_load_dwordx4 v[18:21], v201, s[100:101] nt
	s_add_u32 s100, s22, 0x80300
	s_addc_u32 s101, s90, 0
	global_load_dwordx4 v[14:17], v201, s[100:101] nt
	s_setprio 1
	s_waitcnt lgkmcnt(1)
	v_mfma_f32_16x16x32_f16 v[90:93], v[34:37], v[206:209], v[90:93]
	v_mfma_f32_16x16x32_f16 v[102:105], v[34:37], v[230:233], v[102:105]
	v_mfma_f32_16x16x32_f16 v[106:109], v[34:37], v[234:237], v[106:109]
	v_mfma_f32_16x16x32_f16 v[82:85], v[34:37], v[238:241], v[82:85]
	v_mfma_f32_16x16x32_f16 v[110:113], v[38:41], v[206:209], v[110:113]
	v_mfma_f32_16x16x32_f16 v[114:117], v[38:41], v[230:233], v[114:117]
	v_mfma_f32_16x16x32_f16 v[118:121], v[38:41], v[234:237], v[118:121]
	v_mfma_f32_16x16x32_f16 v[86:89], v[38:41], v[238:241], v[86:89]
	s_setprio 0
	ds_read_b128 v[34:37], v130 offset:4096
	ds_read_b128 v[38:41], v130 offset:6144
	v_cvt_pk_f16_f32 v1, v12, v13
	v_cvt_pk_f16_f32 v0, v10, v11
	ds_write_b64 v100, v[0:1] offset:53248
	s_add_u32 s80, s22, 0xa0300
	s_addc_u32 s81, s90, 0
	s_add_u32 s100, s22, 0xa0300
	s_addc_u32 s101, s90, 0
	global_load_dwordx4 v[10:13], v201, s[100:101] nt
	s_setprio 1
	s_waitcnt lgkmcnt(1)
	v_mfma_f32_16x16x32_f16 v[146:149], v[34:37], v[234:237], v[146:149]
	v_mfma_f32_16x16x32_f16 v[122:125], v[34:37], v[238:241], v[122:125]
	v_mfma_f32_16x16x32_f16 v[134:137], v[38:41], v[238:241], v[134:137]
	v_mfma_f32_16x16x32_f16 v[138:141], v[34:37], v[206:209], v[138:141]
	v_mfma_f32_16x16x32_f16 v[142:145], v[34:37], v[230:233], v[142:145]
	v_mfma_f32_16x16x32_f16 v[150:153], v[38:41], v[206:209], v[150:153]
	v_mfma_f32_16x16x32_f16 v[154:157], v[38:41], v[230:233], v[154:157]
	v_mfma_f32_16x16x32_f16 v[158:161], v[38:41], v[234:237], v[158:161]
	s_setprio 0
	ds_read_b128 v[38:41], v130 offset:8192
	ds_read_b128 v[242:245], v130 offset:10240
	v_cvt_pk_f16_f32 v1, v8, v9
	v_cvt_pk_f16_f32 v0, v6, v7
	ds_write_b64 v100, v[0:1] offset:57344
	s_add_u32 s80, s22, 0xc0300
	s_addc_u32 s81, s90, 0
	s_add_u32 s100, s22, 0xc0300
	s_addc_u32 s101, s90, 0
	global_load_dwordx4 v[34:37], v201, s[100:101] nt
	s_setprio 1
	s_waitcnt lgkmcnt(1)
	v_mfma_f32_16x16x32_f16 v[6:9], v[38:41], v[206:209], v[170:173]
	v_mfma_f32_16x16x32_f16 v[170:173], v[38:41], v[230:233], v[174:177]
	v_mfma_f32_16x16x32_f16 v[174:177], v[38:41], v[234:237], v[178:181]
	v_mfma_f32_16x16x32_f16 v[162:165], v[38:41], v[238:241], v[162:165]
	v_mfma_f32_16x16x32_f16 v[178:181], v[242:245], v[206:209], v[182:185]
	v_mfma_f32_16x16x32_f16 v[182:185], v[242:245], v[230:233], v[186:189]
	v_mfma_f32_16x16x32_f16 v[186:189], v[242:245], v[234:237], v[190:193]
	v_mfma_f32_16x16x32_f16 v[166:169], v[242:245], v[238:241], v[166:169]
	s_setprio 0
	s_nop 0
	ds_read_b128 v[190:193], v130 offset:12288
	ds_read_b128 v[242:245], v130 offset:14336
	v_cvt_pk_f16_f32 v1, v4, v5
	v_cvt_pk_f16_f32 v0, v2, v3
	ds_write_b64 v100, v[0:1] offset:61440
	s_add_u32 s80, s22, 0xe0300
	s_addc_u32 s81, s90, 0
	s_add_u32 s100, s22, 0xe0300
	s_addc_u32 s101, s90, 0
	global_load_dwordx4 v[38:41], v201, s[100:101] nt
	s_setprio 1
	s_waitcnt lgkmcnt(1)
	v_mfma_f32_16x16x32_f16 v[78:81], v[242:245], v[238:241], v[78:81]
	v_mfma_f32_16x16x32_f16 v[210:213], v[190:193], v[206:209], v[210:213]
	v_mfma_f32_16x16x32_f16 v[214:217], v[190:193], v[230:233], v[214:217]
	v_mfma_f32_16x16x32_f16 v[218:221], v[190:193], v[234:237], v[218:221]
	v_mfma_f32_16x16x32_f16 v[190:193], v[190:193], v[238:241], v[202:205]
	v_mfma_f32_16x16x32_f16 v[202:205], v[242:245], v[206:209], v[222:225]
	v_mfma_f32_16x16x32_f16 v[206:209], v[242:245], v[230:233], v[226:229]
	v_mfma_f32_16x16x32_f16 v[222:225], v[242:245], v[234:237], v[74:77]
	s_setprio 0
	s_waitcnt vmcnt(6)
	s_waitcnt lgkmcnt(0)
	s_barrier
	ds_read_b128 v[226:229], v131 offset:32768
	ds_read_b128 v[230:233], v131 offset:34816
	ds_read_b128 v[234:237], v131 offset:36864
	ds_read_b128 v[238:241], v131 offset:38912
	ds_read_b128 v[74:77], v129 offset:32768
	ds_read_b128 v[242:245], v129 offset:34816
	s_add_u32 s80, s22, 0x400
	s_addc_u32 s81, s90, 0
	v_lshl_add_u64 v[198:199], s[28:29], 0, v[196:197]
	v_readfirstlane_b32 s70, v94
	s_mov_b32 m0, s70
	v_cvt_pk_f16_f32 v1, v72, v73
	global_load_lds_dwordx4 v[198:199], off
	v_cvt_pk_f16_f32 v0, v70, v71
	ds_write_b64 v100, v[0:1]
	s_setprio 1
	s_waitcnt lgkmcnt(1)
	v_mfma_f32_16x16x32_f16 v[70:73], v[74:77], v[226:229], v[90:93]
	v_mfma_f32_16x16x32_f16 v[90:93], v[74:77], v[230:233], v[102:105]
	v_mfma_f32_16x16x32_f16 v[104:107], v[74:77], v[234:237], v[106:109]
	v_mfma_f32_16x16x32_f16 v[82:85], v[74:77], v[238:241], v[82:85]
	v_mfma_f32_16x16x32_f16 v[108:111], v[242:245], v[226:229], v[110:113]
	v_mfma_f32_16x16x32_f16 v[112:115], v[242:245], v[230:233], v[114:117]
	v_mfma_f32_16x16x32_f16 v[116:119], v[242:245], v[234:237], v[118:121]
	v_mfma_f32_16x16x32_f16 v[86:89], v[242:245], v[238:241], v[86:89]
	s_setprio 0
	ds_read_b128 v[74:77], v129 offset:36864
	ds_read_b128 v[242:245], v129 offset:38912
	v_add_u32_e32 v99, 0x2000, v94
	v_lshl_add_u64 v[4:5], v[198:199], 0, s[58:59]
	v_readfirstlane_b32 s73, v99
	s_mov_b32 m0, s73
	s_nop 0
	global_load_lds_dwordx4 v[4:5], off
	v_cvt_pk_f16_f32 v5, v44, v45
	v_cvt_pk_f16_f32 v4, v42, v43
	ds_write_b64 v100, v[4:5] offset:4096
	s_add_u32 s80, s22, 0x20400
	s_addc_u32 s81, s90, 0
	s_add_u32 s100, s22, 0x400
	s_addc_u32 s101, s90, 0
	global_load_dwordx4 v[0:3], v201, s[100:101] nt
	s_setprio 1
	s_waitcnt lgkmcnt(1)
	v_mfma_f32_16x16x32_f16 v[146:149], v[74:77], v[234:237], v[146:149]
	v_mfma_f32_16x16x32_f16 v[120:123], v[74:77], v[238:241], v[122:125]
	v_mfma_f32_16x16x32_f16 v[124:127], v[242:245], v[226:229], v[150:153]
	v_mfma_f32_16x16x32_f16 v[134:137], v[242:245], v[238:241], v[134:137]
	v_mfma_f32_16x16x32_f16 v[138:141], v[74:77], v[226:229], v[138:141]
	v_mfma_f32_16x16x32_f16 v[142:145], v[74:77], v[230:233], v[142:145]
	v_mfma_f32_16x16x32_f16 v[150:153], v[242:245], v[230:233], v[154:157]
	v_mfma_f32_16x16x32_f16 v[154:157], v[242:245], v[234:237], v[158:161]
	s_setprio 0
	ds_read_b128 v[74:77], v129 offset:40960
	s_nop 0
	ds_read_b128 v[158:161], v129 offset:43008
	v_add_u32_e32 v101, 0x4000, v94
	v_lshl_add_u64 v[4:5], v[198:199], 0, s[60:61]
	v_readfirstlane_b32 s91, v101
	s_mov_b32 m0, s91
	s_nop 0
	global_load_lds_dwordx4 v[4:5], off
	v_cvt_pk_f16_f32 v5, v48, v49
	v_cvt_pk_f16_f32 v4, v46, v47
	ds_write_b64 v100, v[4:5] offset:8192
	s_add_u32 s80, s22, 0x40400
	s_addc_u32 s81, s90, 0
	s_add_u32 s100, s22, 0x20400
	s_addc_u32 s101, s90, 0
	global_load_dwordx4 v[42:45], v201, s[100:101] nt
	s_setprio 1
	s_waitcnt lgkmcnt(1)
	v_mfma_f32_16x16x32_f16 v[4:7], v[74:77], v[226:229], v[6:9]
	v_mfma_f32_16x16x32_f16 v[170:173], v[74:77], v[230:233], v[170:173]
	v_mfma_f32_16x16x32_f16 v[174:177], v[74:77], v[234:237], v[174:177]
	v_mfma_f32_16x16x32_f16 v[162:165], v[74:77], v[238:241], v[162:165]
	v_mfma_f32_16x16x32_f16 v[178:181], v[158:161], v[226:229], v[178:181]
	v_mfma_f32_16x16x32_f16 v[182:185], v[158:161], v[230:233], v[182:185]
	v_mfma_f32_16x16x32_f16 v[186:189], v[158:161], v[234:237], v[186:189]
	v_mfma_f32_16x16x32_f16 v[158:161], v[158:161], v[238:241], v[166:169]
	s_setprio 0
	s_nop 1
	ds_read_b128 v[166:169], v129 offset:45056
	ds_read_b128 v[242:245], v129 offset:47104
	v_add_u32_e32 v102, 0x6000, v94
	v_lshl_add_u64 v[8:9], v[198:199], 0, s[62:63]
	v_readfirstlane_b32 s92, v102
	s_mov_b32 m0, s92
	s_nop 0
	global_load_lds_dwordx4 v[8:9], off
	v_cvt_pk_f16_f32 v9, v68, v69
	v_cvt_pk_f16_f32 v8, v66, v67
	ds_write_b64 v100, v[8:9] offset:12288
	s_add_u32 s80, s22, 0x60400
	s_addc_u32 s81, s90, 0
	s_add_u32 s100, s22, 0x40400
	s_addc_u32 s101, s90, 0
	global_load_dwordx4 v[46:49], v201, s[100:101] nt
	s_setprio 1
	s_waitcnt lgkmcnt(1)
	v_mfma_f32_16x16x32_f16 v[66:69], v[166:169], v[226:229], v[210:213]
	v_mfma_f32_16x16x32_f16 v[210:213], v[166:169], v[230:233], v[214:217]
	v_mfma_f32_16x16x32_f16 v[214:217], v[166:169], v[234:237], v[218:221]
	v_mfma_f32_16x16x32_f16 v[166:169], v[166:169], v[238:241], v[190:193]
	v_mfma_f32_16x16x32_f16 v[190:193], v[242:245], v[226:229], v[202:205]
	v_mfma_f32_16x16x32_f16 v[202:205], v[242:245], v[230:233], v[206:209]
	v_mfma_f32_16x16x32_f16 v[206:209], v[242:245], v[234:237], v[222:225]
	v_mfma_f32_16x16x32_f16 v[218:221], v[242:245], v[238:241], v[78:81]
	s_setprio 0
	s_nop 0
	ds_read_b128 v[222:225], v128 offset:32768
	ds_read_b128 v[226:229], v128 offset:34816
	ds_read_b128 v[230:233], v128 offset:36864
	ds_read_b128 v[234:237], v128 offset:38912
	ds_read_b128 v[238:241], v130 offset:32768
	ds_read_b128 v[242:245], v130 offset:34816
	v_cvt_pk_f16_f32 v9, v64, v65
	v_cvt_pk_f16_f32 v8, v62, v63
	ds_write_b64 v100, v[8:9] offset:16384
	s_add_u32 s80, s22, 0x80400
	s_addc_u32 s81, s90, 0
	s_add_u32 s100, s22, 0x60400
	s_addc_u32 s101, s90, 0
	global_load_dwordx4 v[74:77], v201, s[100:101] nt
	s_add_u32 s100, s22, 0x80400
	s_addc_u32 s101, s90, 0
	global_load_dwordx4 v[78:81], v201, s[100:101] nt
	s_setprio 1
	s_waitcnt lgkmcnt(1)
	v_mfma_f32_16x16x32_f16 v[62:65], v[238:241], v[222:225], v[70:73]
	v_mfma_f32_16x16x32_f16 v[70:73], v[238:241], v[226:229], v[90:93]
	v_mfma_f32_16x16x32_f16 v[104:107], v[238:241], v[230:233], v[104:107]
	v_mfma_f32_16x16x32_f16 v[108:111], v[242:245], v[222:225], v[108:111]
	v_mfma_f32_16x16x32_f16 v[112:115], v[242:245], v[226:229], v[112:115]
	v_mfma_f32_16x16x32_f16 v[116:119], v[242:245], v[230:233], v[116:119]
	v_mfma_f32_16x16x32_f16 v[238:241], v[238:241], v[234:237], v[82:85]
	v_mfma_f32_16x16x32_f16 v[242:245], v[242:245], v[234:237], v[86:89]
	s_setprio 0
	s_nop 1
	ds_read_b128 v[86:89], v130 offset:36864
	ds_read_b128 v[90:93], v130 offset:38912
	v_cvt_pk_f16_f32 v9, v60, v61
	v_cvt_pk_f16_f32 v8, v58, v59
	ds_write_b64 v100, v[8:9] offset:20480
	s_add_u32 s80, s22, 0xa0400
	s_addc_u32 s81, s90, 0
	s_add_u32 s100, s22, 0xa0400
	s_addc_u32 s101, s90, 0
	global_load_dwordx4 v[82:85], v201, s[100:101] nt
	s_setprio 1
	s_waitcnt lgkmcnt(1)
	v_mfma_f32_16x16x32_f16 v[58:61], v[86:89], v[222:225], v[138:141]
	v_mfma_f32_16x16x32_f16 v[138:141], v[86:89], v[226:229], v[142:145]
	v_mfma_f32_16x16x32_f16 v[142:145], v[86:89], v[230:233], v[146:149]
	v_mfma_f32_16x16x32_f16 v[120:123], v[86:89], v[234:237], v[120:123]
	v_mfma_f32_16x16x32_f16 v[124:127], v[90:93], v[222:225], v[124:127]
	v_mfma_f32_16x16x32_f16 v[146:149], v[90:93], v[226:229], v[150:153]
	v_mfma_f32_16x16x32_f16 v[134:137], v[90:93], v[234:237], v[134:137]
	v_mfma_f32_16x16x32_f16 v[150:153], v[90:93], v[230:233], v[154:157]
	s_setprio 0
	ds_read_b128 v[90:93], v130 offset:40960
	s_nop 0
	ds_read_b128 v[154:157], v130 offset:43008
	v_cvt_pk_f16_f32 v9, v56, v57
	v_cvt_pk_f16_f32 v8, v54, v55
	ds_write_b64 v100, v[8:9] offset:24576
	s_add_u32 s80, s22, 0xc0400
	s_addc_u32 s81, s90, 0
	s_add_u32 s100, s22, 0xc0400
	s_addc_u32 s101, s90, 0
	global_load_dwordx4 v[86:89], v201, s[100:101] nt
	s_setprio 1
	s_waitcnt lgkmcnt(1)
	v_mfma_f32_16x16x32_f16 v[246:249], v[90:93], v[222:225], v[4:7]
	v_mfma_f32_16x16x32_f16 v[170:173], v[90:93], v[226:229], v[170:173]
	v_mfma_f32_16x16x32_f16 v[174:177], v[90:93], v[230:233], v[174:177]
	v_mfma_f32_16x16x32_f16 v[162:165], v[90:93], v[234:237], v[162:165]
	v_mfma_f32_16x16x32_f16 v[178:181], v[154:157], v[222:225], v[178:181]
	v_mfma_f32_16x16x32_f16 v[182:185], v[154:157], v[226:229], v[182:185]
	v_mfma_f32_16x16x32_f16 v[186:189], v[154:157], v[230:233], v[186:189]
	v_mfma_f32_16x16x32_f16 v[154:157], v[154:157], v[234:237], v[158:161]
	s_setprio 0
	ds_read_b128 v[4:7], v130 offset:45056
	ds_read_b128 v[54:57], v130 offset:47104
	v_cvt_pk_f16_f32 v9, v52, v53
	v_cvt_pk_f16_f32 v8, v50, v51
	ds_write_b64 v100, v[8:9] offset:28672
	s_add_u32 s80, s22, 0xe0400
	s_addc_u32 s81, s90, 0
	s_add_u32 s100, s22, 0xe0400
	s_addc_u32 s101, s90, 0
	global_load_dwordx4 v[90:93], v201, s[100:101] nt
	s_setprio 1
	s_waitcnt lgkmcnt(1)
	v_mfma_f32_16x16x32_f16 v[66:69], v[4:7], v[222:225], v[66:69]
	v_mfma_f32_16x16x32_f16 v[158:161], v[4:7], v[226:229], v[210:213]
	v_mfma_f32_16x16x32_f16 v[210:213], v[4:7], v[230:233], v[214:217]
	v_mfma_f32_16x16x32_f16 v[166:169], v[4:7], v[234:237], v[166:169]
	v_mfma_f32_16x16x32_f16 v[190:193], v[54:57], v[222:225], v[190:193]
	v_mfma_f32_16x16x32_f16 v[202:205], v[54:57], v[226:229], v[202:205]
	v_mfma_f32_16x16x32_f16 v[206:209], v[54:57], v[230:233], v[206:209]
	v_mfma_f32_16x16x32_f16 v[214:217], v[54:57], v[234:237], v[218:221]
	s_setprio 0
	s_waitcnt vmcnt(6)
	s_waitcnt lgkmcnt(0)
	s_barrier
	s_nop 0
	ds_read_b128 v[218:221], v131
	ds_read_b128 v[222:225], v131 offset:2048
	ds_read_b128 v[226:229], v131 offset:4096
	ds_read_b128 v[230:233], v131 offset:6144
	ds_read_b128 v[50:53], v129
	ds_read_b128 v[54:57], v129 offset:2048
	s_add_u32 s80, s22, 0x500
	v_lshl_add_u64 v[8:9], s[30:31], 0, v[196:197]
	s_addc_u32 s81, s90, 0
	s_mov_b32 m0, s0
	v_cvt_pk_f16_f32 v5, v32, v33
	global_load_lds_dwordx4 v[8:9], off
	v_cvt_pk_f16_f32 v4, v30, v31
	ds_write_b64 v100, v[4:5] offset:32768
	s_setprio 1
	s_waitcnt lgkmcnt(1)
	v_mfma_f32_16x16x32_f16 v[30:33], v[50:53], v[218:221], v[62:65]
	v_mfma_f32_16x16x32_f16 v[70:73], v[50:53], v[222:225], v[70:73]
	v_mfma_f32_16x16x32_f16 v[104:107], v[50:53], v[226:229], v[104:107]
	v_mfma_f32_16x16x32_f16 v[108:111], v[54:57], v[218:221], v[108:111]
	v_mfma_f32_16x16x32_f16 v[112:115], v[54:57], v[222:225], v[112:115]
	v_mfma_f32_16x16x32_f16 v[116:119], v[54:57], v[226:229], v[116:119]
	v_mfma_f32_16x16x32_f16 v[234:237], v[50:53], v[230:233], v[238:241]
	v_mfma_f32_16x16x32_f16 v[238:241], v[54:57], v[230:233], v[242:245]
	s_setprio 0
	ds_read_b128 v[54:57], v129 offset:4096
	ds_read_b128 v[62:65], v129 offset:6144
	s_mov_b32 m0, s1
	v_lshl_add_u64 v[50:51], v[8:9], 0, s[58:59]
	global_load_lds_dwordx4 v[50:51], off
	v_cvt_pk_f16_f32 v29, v28, v29
	v_cvt_pk_f16_f32 v28, v26, v27
	ds_write_b64 v100, v[28:29] offset:36864
	s_add_u32 s0, s22, 0x20500
	s_addc_u32 s1, s90, 0
	s_add_u32 s100, s22, 0x500
	s_addc_u32 s101, s90, 0
	global_load_dwordx4 v[4:7], v201, s[100:101] nt
	s_setprio 1
	s_waitcnt lgkmcnt(1)
	v_mfma_f32_16x16x32_f16 v[26:29], v[54:57], v[218:221], v[58:61]
	v_mfma_f32_16x16x32_f16 v[120:123], v[54:57], v[230:233], v[120:123]
	v_mfma_f32_16x16x32_f16 v[124:127], v[62:65], v[218:221], v[124:127]
	v_mfma_f32_16x16x32_f16 v[146:149], v[62:65], v[222:225], v[146:149]
	v_mfma_f32_16x16x32_f16 v[134:137], v[62:65], v[230:233], v[134:137]
	v_mfma_f32_16x16x32_f16 v[138:141], v[54:57], v[222:225], v[138:141]
	v_mfma_f32_16x16x32_f16 v[142:145], v[54:57], v[226:229], v[142:145]
	v_mfma_f32_16x16x32_f16 v[150:153], v[62:65], v[226:229], v[150:153]
	s_setprio 0
	ds_read_b128 v[58:61], v129 offset:8192
	ds_read_b128 v[62:65], v129 offset:10240
	s_mov_b32 m0, s71
	v_lshl_add_u64 v[54:55], v[8:9], 0, s[60:61]
	global_load_lds_dwordx4 v[54:55], off
	v_cvt_pk_f16_f32 v25, v24, v25
	v_cvt_pk_f16_f32 v24, v22, v23
	ds_write_b64 v100, v[24:25] offset:40960
	s_add_u32 s0, s22, 0x40500
	s_addc_u32 s1, s90, 0
	s_add_u32 s100, s22, 0x20500
	s_addc_u32 s101, s90, 0
	global_load_dwordx4 v[50:53], v201, s[100:101] nt
	s_setprio 1
	s_waitcnt lgkmcnt(1)
	v_mfma_f32_16x16x32_f16 v[22:25], v[58:61], v[218:221], v[246:249]
	v_mfma_f32_16x16x32_f16 v[170:173], v[58:61], v[222:225], v[170:173]
	v_mfma_f32_16x16x32_f16 v[174:177], v[58:61], v[226:229], v[174:177]
	v_mfma_f32_16x16x32_f16 v[162:165], v[58:61], v[230:233], v[162:165]
	v_mfma_f32_16x16x32_f16 v[178:181], v[62:65], v[218:221], v[178:181]
	v_mfma_f32_16x16x32_f16 v[182:185], v[62:65], v[222:225], v[182:185]
	v_mfma_f32_16x16x32_f16 v[186:189], v[62:65], v[226:229], v[186:189]
	v_mfma_f32_16x16x32_f16 v[154:157], v[62:65], v[230:233], v[154:157]
	s_setprio 0
	ds_read_b128 v[62:65], v129 offset:12288
	ds_read_b128 v[242:245], v129 offset:14336
	s_mov_b32 m0, s72
	v_lshl_add_u64 v[8:9], v[8:9], 0, s[62:63]
	global_load_lds_dwordx4 v[8:9], off
	v_cvt_pk_f16_f32 v9, v20, v21
	v_cvt_pk_f16_f32 v8, v18, v19
	ds_write_b64 v100, v[8:9] offset:45056
	s_add_u32 s0, s22, 0x60500
	s_addc_u32 s1, s90, 0
	s_add_u32 s100, s22, 0x40500
	s_addc_u32 s101, s90, 0
	global_load_dwordx4 v[54:57], v201, s[100:101] nt
	s_setprio 1
	s_waitcnt lgkmcnt(1)
	v_mfma_f32_16x16x32_f16 v[18:21], v[62:65], v[218:221], v[66:69]
	v_mfma_f32_16x16x32_f16 v[158:161], v[62:65], v[222:225], v[158:161]
	v_mfma_f32_16x16x32_f16 v[210:213], v[62:65], v[226:229], v[210:213]
	v_mfma_f32_16x16x32_f16 v[166:169], v[62:65], v[230:233], v[166:169]
	v_mfma_f32_16x16x32_f16 v[190:193], v[242:245], v[218:221], v[190:193]
	v_mfma_f32_16x16x32_f16 v[202:205], v[242:245], v[222:225], v[202:205]
	v_mfma_f32_16x16x32_f16 v[206:209], v[242:245], v[226:229], v[206:209]
	v_mfma_f32_16x16x32_f16 v[214:217], v[242:245], v[230:233], v[214:217]
	s_setprio 0
	ds_read_b128 v[218:221], v128
	ds_read_b128 v[222:225], v128 offset:2048
	ds_read_b128 v[226:229], v128 offset:4096
	ds_read_b128 v[230:233], v128 offset:6144
	ds_read_b128 v[66:69], v130
	ds_read_b128 v[242:245], v130 offset:2048
	v_cvt_pk_f16_f32 v9, v16, v17
	v_cvt_pk_f16_f32 v8, v14, v15
	ds_write_b64 v100, v[8:9] offset:49152
	s_add_u32 s0, s22, 0x80500
	s_addc_u32 s1, s90, 0
	s_add_u32 s100, s22, 0x60500
	s_addc_u32 s101, s90, 0
	global_load_dwordx4 v[58:61], v201, s[100:101] nt
	s_add_u32 s100, s22, 0x80500
	s_addc_u32 s101, s90, 0
	global_load_dwordx4 v[62:65], v201, s[100:101] nt
	s_setprio 1
	s_waitcnt lgkmcnt(1)
	v_mfma_f32_16x16x32_f16 v[14:17], v[66:69], v[218:221], v[30:33]
	v_mfma_f32_16x16x32_f16 v[30:33], v[66:69], v[222:225], v[70:73]
	v_mfma_f32_16x16x32_f16 v[104:107], v[66:69], v[226:229], v[104:107]
	v_mfma_f32_16x16x32_f16 v[108:111], v[242:245], v[218:221], v[108:111]
	v_mfma_f32_16x16x32_f16 v[112:115], v[242:245], v[222:225], v[112:115]
	v_mfma_f32_16x16x32_f16 v[116:119], v[242:245], v[226:229], v[116:119]
	v_mfma_f32_16x16x32_f16 v[234:237], v[66:69], v[230:233], v[234:237]
	v_mfma_f32_16x16x32_f16 v[238:241], v[242:245], v[230:233], v[238:241]
	s_setprio 0
	ds_read_b128 v[70:73], v130 offset:4096
	ds_read_b128 v[242:245], v130 offset:6144
	v_cvt_pk_f16_f32 v9, v12, v13
	v_cvt_pk_f16_f32 v8, v10, v11
	ds_write_b64 v100, v[8:9] offset:53248
	s_add_u32 s0, s22, 0xa0500
	s_addc_u32 s1, s90, 0
	s_add_u32 s100, s22, 0xa0500
	s_addc_u32 s101, s90, 0
	global_load_dwordx4 v[66:69], v201, s[100:101] nt
	s_setprio 1
	s_waitcnt lgkmcnt(1)
	v_mfma_f32_16x16x32_f16 v[26:29], v[70:73], v[218:221], v[26:29]
	v_mfma_f32_16x16x32_f16 v[120:123], v[70:73], v[230:233], v[120:123]
	v_mfma_f32_16x16x32_f16 v[124:127], v[242:245], v[218:221], v[124:127]
	v_mfma_f32_16x16x32_f16 v[146:149], v[242:245], v[222:225], v[146:149]
	v_mfma_f32_16x16x32_f16 v[134:137], v[242:245], v[230:233], v[134:137]
	v_mfma_f32_16x16x32_f16 v[138:141], v[70:73], v[222:225], v[138:141]
	v_mfma_f32_16x16x32_f16 v[142:145], v[70:73], v[226:229], v[142:145]
	v_mfma_f32_16x16x32_f16 v[150:153], v[242:245], v[226:229], v[150:153]
	s_setprio 0
	ds_read_b128 v[8:11], v130 offset:8192
	ds_read_b128 v[242:245], v130 offset:10240
	v_cvt_pk_f16_f32 v13, v36, v37
	v_cvt_pk_f16_f32 v12, v34, v35
	ds_write_b64 v100, v[12:13] offset:57344
	s_add_u32 s0, s22, 0xc0500
	s_addc_u32 s1, s90, 0
	s_add_u32 s100, s22, 0xc0500
	s_addc_u32 s101, s90, 0
	global_load_dwordx4 v[70:73], v201, s[100:101] nt
	s_setprio 1
	s_waitcnt lgkmcnt(1)
	v_mfma_f32_16x16x32_f16 v[22:25], v[8:11], v[218:221], v[22:25]
	v_mfma_f32_16x16x32_f16 v[170:173], v[8:11], v[222:225], v[170:173]
	v_mfma_f32_16x16x32_f16 v[174:177], v[8:11], v[226:229], v[174:177]
	v_mfma_f32_16x16x32_f16 v[162:165], v[8:11], v[230:233], v[162:165]
	v_mfma_f32_16x16x32_f16 v[178:181], v[242:245], v[218:221], v[178:181]
	v_mfma_f32_16x16x32_f16 v[182:185], v[242:245], v[222:225], v[182:185]
	v_mfma_f32_16x16x32_f16 v[186:189], v[242:245], v[226:229], v[186:189]
	v_mfma_f32_16x16x32_f16 v[154:157], v[242:245], v[230:233], v[154:157]
	s_setprio 0
	ds_read_b128 v[8:11], v130 offset:12288
	ds_read_b128 v[242:245], v130 offset:14336
	v_cvt_pk_f16_f32 v13, v40, v41
	v_cvt_pk_f16_f32 v12, v38, v39
	ds_write_b64 v100, v[12:13] offset:61440
	s_add_u32 s0, s22, 0xe0500
	s_addc_u32 s1, s90, 0
	s_add_u32 s100, s22, 0xe0500
	s_addc_u32 s101, s90, 0
	global_load_dwordx4 v[36:39], v201, s[100:101] nt
	s_setprio 1
	s_waitcnt lgkmcnt(1)
	v_mfma_f32_16x16x32_f16 v[246:249], v[8:11], v[218:221], v[18:21]
	v_mfma_f32_16x16x32_f16 v[158:161], v[8:11], v[222:225], v[158:161]
	v_mfma_f32_16x16x32_f16 v[210:213], v[8:11], v[226:229], v[210:213]
	v_mfma_f32_16x16x32_f16 v[166:169], v[8:11], v[230:233], v[166:169]
	v_mfma_f32_16x16x32_f16 v[190:193], v[242:245], v[218:221], v[190:193]
	v_mfma_f32_16x16x32_f16 v[202:205], v[242:245], v[222:225], v[202:205]
	v_mfma_f32_16x16x32_f16 v[206:209], v[242:245], v[226:229], v[206:209]
	v_mfma_f32_16x16x32_f16 v[214:217], v[242:245], v[230:233], v[214:217]
	s_setprio 0
	s_waitcnt vmcnt(6)
	s_waitcnt lgkmcnt(0)
	s_barrier
	ds_read_b128 v[218:221], v131 offset:32768
	ds_read_b128 v[222:225], v131 offset:34816
	ds_read_b128 v[226:229], v131 offset:36864
	ds_read_b128 v[230:233], v131 offset:38912
	ds_read_b128 v[8:11], v129 offset:32768
	ds_read_b128 v[18:21], v129 offset:34816
	s_add_u32 s0, s22, 0x600
	s_addc_u32 s1, s90, 0
	v_lshl_add_u64 v[34:35], s[34:35], 0, v[196:197]
	s_mov_b32 m0, s70
	v_cvt_pk_f16_f32 v3, v2, v3
	global_load_lds_dwordx4 v[34:35], off
	v_cvt_pk_f16_f32 v2, v0, v1
	ds_write_b64 v100, v[2:3]
	s_setprio 1
	s_waitcnt lgkmcnt(1)
	v_mfma_f32_16x16x32_f16 v[30:33], v[8:11], v[222:225], v[30:33]
	v_mfma_f32_16x16x32_f16 v[104:107], v[8:11], v[226:229], v[104:107]
	v_mfma_f32_16x16x32_f16 v[108:111], v[18:21], v[218:221], v[108:111]
	v_mfma_f32_16x16x32_f16 v[112:115], v[18:21], v[222:225], v[112:115]
	v_mfma_f32_16x16x32_f16 v[116:119], v[18:21], v[226:229], v[116:119]
	v_mfma_f32_16x16x32_f16 v[242:245], v[8:11], v[218:221], v[14:17]
	v_mfma_f32_16x16x32_f16 v[234:237], v[8:11], v[230:233], v[234:237]
	v_mfma_f32_16x16x32_f16 v[238:241], v[18:21], v[230:233], v[238:241]
	s_setprio 0
	ds_read_b128 v[12:15], v129 offset:36864
	ds_read_b128 v[16:19], v129 offset:38912
	s_mov_b32 m0, s73
	v_lshl_add_u64 v[8:9], v[34:35], 0, s[58:59]
	global_load_lds_dwordx4 v[8:9], off
	v_cvt_pk_f16_f32 v9, v44, v45
	v_cvt_pk_f16_f32 v8, v42, v43
	ds_write_b64 v100, v[8:9] offset:4096
	s_add_u32 s0, s22, 0x20600
	s_addc_u32 s1, s90, 0
	s_add_u32 s100, s22, 0x600
	s_addc_u32 s101, s90, 0
	global_load_dwordx4 v[0:3], v201, s[100:101] nt
	s_setprio 1
	s_waitcnt lgkmcnt(1)
	v_mfma_f32_16x16x32_f16 v[40:43], v[12:15], v[218:221], v[26:29]
	v_mfma_f32_16x16x32_f16 v[120:123], v[12:15], v[230:233], v[120:123]
	v_mfma_f32_16x16x32_f16 v[124:127], v[16:19], v[218:221], v[124:127]
	v_mfma_f32_16x16x32_f16 v[146:149], v[16:19], v[222:225], v[146:149]
	v_mfma_f32_16x16x32_f16 v[134:137], v[16:19], v[230:233], v[134:137]
	v_mfma_f32_16x16x32_f16 v[138:141], v[12:15], v[222:225], v[138:141]
	v_mfma_f32_16x16x32_f16 v[142:145], v[12:15], v[226:229], v[142:145]
	v_mfma_f32_16x16x32_f16 v[150:153], v[16:19], v[226:229], v[150:153]
	s_setprio 0
	ds_read_b128 v[16:19], v129 offset:40960
	ds_read_b128 v[26:29], v129 offset:43008
	s_mov_b32 m0, s91
	v_lshl_add_u64 v[12:13], v[34:35], 0, s[60:61]
	global_load_lds_dwordx4 v[12:13], off
	v_cvt_pk_f16_f32 v13, v48, v49
	v_cvt_pk_f16_f32 v12, v46, v47
	ds_write_b64 v100, v[12:13] offset:8192
	s_add_u32 s0, s22, 0x40600
	s_addc_u32 s1, s90, 0
	s_add_u32 s100, s22, 0x20600
	s_addc_u32 s101, s90, 0
	global_load_dwordx4 v[8:11], v201, s[100:101] nt
	s_setprio 1
	s_waitcnt lgkmcnt(1)
	v_mfma_f32_16x16x32_f16 v[44:47], v[16:19], v[218:221], v[22:25]
	v_mfma_f32_16x16x32_f16 v[170:173], v[16:19], v[222:225], v[170:173]
	v_mfma_f32_16x16x32_f16 v[174:177], v[16:19], v[226:229], v[174:177]
	v_mfma_f32_16x16x32_f16 v[162:165], v[16:19], v[230:233], v[162:165]
	v_mfma_f32_16x16x32_f16 v[178:181], v[26:29], v[218:221], v[178:181]
	v_mfma_f32_16x16x32_f16 v[182:185], v[26:29], v[222:225], v[182:185]
	v_mfma_f32_16x16x32_f16 v[186:189], v[26:29], v[226:229], v[186:189]
	v_mfma_f32_16x16x32_f16 v[154:157], v[26:29], v[230:233], v[154:157]
	s_setprio 0
	ds_read_b128 v[20:23], v129 offset:45056
	ds_read_b128 v[24:27], v129 offset:47104
	s_mov_b32 m0, s92
	v_lshl_add_u64 v[16:17], v[34:35], 0, s[62:63]
	global_load_lds_dwordx4 v[16:17], off
	v_cvt_pk_f16_f32 v17, v76, v77
	v_cvt_pk_f16_f32 v16, v74, v75
	ds_write_b64 v100, v[16:17] offset:12288
	s_add_u32 s0, s22, 0x60600
	s_addc_u32 s1, s90, 0
	s_add_u32 s100, s22, 0x40600
	s_addc_u32 s101, s90, 0
	global_load_dwordx4 v[12:15], v201, s[100:101] nt
	s_setprio 1
	s_waitcnt lgkmcnt(1)
	v_mfma_f32_16x16x32_f16 v[74:77], v[20:23], v[218:221], v[246:249]
	v_mfma_f32_16x16x32_f16 v[158:161], v[20:23], v[222:225], v[158:161]
	v_mfma_f32_16x16x32_f16 v[210:213], v[20:23], v[226:229], v[210:213]
	v_mfma_f32_16x16x32_f16 v[166:169], v[20:23], v[230:233], v[166:169]
	v_mfma_f32_16x16x32_f16 v[190:193], v[24:27], v[218:221], v[190:193]
	v_mfma_f32_16x16x32_f16 v[202:205], v[24:27], v[222:225], v[202:205]
	v_mfma_f32_16x16x32_f16 v[206:209], v[24:27], v[226:229], v[206:209]
	v_mfma_f32_16x16x32_f16 v[214:217], v[24:27], v[230:233], v[214:217]
	s_setprio 0
	ds_read_b128 v[218:221], v128 offset:32768
	ds_read_b128 v[222:225], v128 offset:34816
	ds_read_b128 v[226:229], v128 offset:36864
	ds_read_b128 v[230:233], v128 offset:38912
	ds_read_b128 v[24:27], v130 offset:32768
	ds_read_b128 v[246:249], v130 offset:34816
	v_cvt_pk_f16_f32 v21, v80, v81
	v_cvt_pk_f16_f32 v20, v78, v79
	ds_write_b64 v100, v[20:21] offset:16384
	s_add_u32 s0, s22, 0x80600
	s_addc_u32 s1, s90, 0
	s_add_u32 s100, s22, 0x60600
	s_addc_u32 s101, s90, 0
	global_load_dwordx4 v[16:19], v201, s[100:101] nt
	s_add_u32 s100, s22, 0x80600
	s_addc_u32 s101, s90, 0
	global_load_dwordx4 v[20:23], v201, s[100:101] nt
	s_setprio 1
	s_waitcnt lgkmcnt(1)
	v_mfma_f32_16x16x32_f16 v[78:81], v[24:27], v[218:221], v[242:245]
	v_mfma_f32_16x16x32_f16 v[104:107], v[24:27], v[226:229], v[104:107]
	v_mfma_f32_16x16x32_f16 v[108:111], v[246:249], v[218:221], v[108:111]
	v_mfma_f32_16x16x32_f16 v[112:115], v[246:249], v[222:225], v[112:115]
	v_mfma_f32_16x16x32_f16 v[116:119], v[246:249], v[226:229], v[116:119]
	v_mfma_f32_16x16x32_f16 v[242:245], v[24:27], v[222:225], v[30:33]
	v_mfma_f32_16x16x32_f16 v[234:237], v[24:27], v[230:233], v[234:237]
	v_mfma_f32_16x16x32_f16 v[238:241], v[246:249], v[230:233], v[238:241]
	s_setprio 0
	ds_read_b128 v[28:31], v130 offset:36864
	ds_read_b128 v[32:35], v130 offset:38912
	v_cvt_pk_f16_f32 v25, v84, v85
	v_cvt_pk_f16_f32 v24, v82, v83
	ds_write_b64 v100, v[24:25] offset:20480
	s_add_u32 s0, s22, 0xa0600
	s_addc_u32 s1, s90, 0
	s_add_u32 s100, s22, 0xa0600
	s_addc_u32 s101, s90, 0
	global_load_dwordx4 v[24:27], v201, s[100:101] nt
	s_setprio 1
	s_waitcnt lgkmcnt(1)
	v_mfma_f32_16x16x32_f16 v[82:85], v[28:31], v[218:221], v[40:43]
	v_mfma_f32_16x16x32_f16 v[120:123], v[28:31], v[230:233], v[120:123]
	v_mfma_f32_16x16x32_f16 v[124:127], v[32:35], v[218:221], v[124:127]
	v_mfma_f32_16x16x32_f16 v[146:149], v[32:35], v[222:225], v[146:149]
	v_mfma_f32_16x16x32_f16 v[134:137], v[32:35], v[230:233], v[134:137]
	v_mfma_f32_16x16x32_f16 v[138:141], v[28:31], v[222:225], v[138:141]
	v_mfma_f32_16x16x32_f16 v[142:145], v[28:31], v[226:229], v[142:145]
	v_mfma_f32_16x16x32_f16 v[150:153], v[32:35], v[226:229], v[150:153]
	s_setprio 0
	ds_read_b128 v[32:35], v130 offset:40960
	ds_read_b128 v[40:43], v130 offset:43008
	v_cvt_pk_f16_f32 v29, v88, v89
	v_cvt_pk_f16_f32 v28, v86, v87
	ds_write_b64 v100, v[28:29] offset:24576
	s_add_u32 s0, s22, 0xc0600
	s_addc_u32 s1, s90, 0
	s_add_u32 s100, s22, 0xc0600
	s_addc_u32 s101, s90, 0
	global_load_dwordx4 v[28:31], v201, s[100:101] nt
	s_setprio 1
	s_waitcnt lgkmcnt(1)
	v_mfma_f32_16x16x32_f16 v[86:89], v[32:35], v[218:221], v[44:47]
	v_mfma_f32_16x16x32_f16 v[170:173], v[32:35], v[222:225], v[170:173]
	v_mfma_f32_16x16x32_f16 v[174:177], v[32:35], v[226:229], v[174:177]
	v_mfma_f32_16x16x32_f16 v[162:165], v[32:35], v[230:233], v[162:165]
	v_mfma_f32_16x16x32_f16 v[178:181], v[40:43], v[218:221], v[178:181]
	v_mfma_f32_16x16x32_f16 v[182:185], v[40:43], v[222:225], v[182:185]
	v_mfma_f32_16x16x32_f16 v[186:189], v[40:43], v[226:229], v[186:189]
	v_mfma_f32_16x16x32_f16 v[154:157], v[40:43], v[230:233], v[154:157]
	s_setprio 0
	ds_read_b128 v[40:43], v130 offset:45056
	ds_read_b128 v[44:47], v130 offset:47104
	v_cvt_pk_f16_f32 v33, v92, v93
	v_cvt_pk_f16_f32 v32, v90, v91
	ds_write_b64 v100, v[32:33] offset:28672
	s_add_u32 s0, s22, 0xe0600
	s_addc_u32 s1, s90, 0
	s_add_u32 s100, s22, 0xe0600
	s_addc_u32 s101, s90, 0
	global_load_dwordx4 v[32:35], v201, s[100:101] nt
	s_setprio 1
	s_waitcnt lgkmcnt(1)
	v_mfma_f32_16x16x32_f16 v[74:77], v[40:43], v[218:221], v[74:77]
	v_mfma_f32_16x16x32_f16 v[90:93], v[40:43], v[222:225], v[158:161]
	v_mfma_f32_16x16x32_f16 v[158:161], v[40:43], v[226:229], v[210:213]
	v_mfma_f32_16x16x32_f16 v[166:169], v[40:43], v[230:233], v[166:169]
	v_mfma_f32_16x16x32_f16 v[190:193], v[44:47], v[218:221], v[190:193]
	v_mfma_f32_16x16x32_f16 v[202:205], v[44:47], v[222:225], v[202:205]
	v_mfma_f32_16x16x32_f16 v[206:209], v[44:47], v[226:229], v[206:209]
	v_mfma_f32_16x16x32_f16 v[210:213], v[44:47], v[230:233], v[214:217]
	s_setprio 0
	s_waitcnt vmcnt(6)
	s_waitcnt lgkmcnt(0)
	s_barrier
	s_nop 0
	ds_read_b128 v[214:217], v131
	ds_read_b128 v[218:221], v131 offset:2048
	ds_read_b128 v[222:225], v131 offset:4096
	ds_read_b128 v[226:229], v131 offset:6144
	ds_read_b128 v[40:43], v129
	ds_read_b128 v[44:47], v129 offset:2048
	s_add_u32 s70, s22, 0x700
	s_addc_u32 s71, s90, 0
	v_lshl_add_u64 v[198:199], s[36:37], 0, v[196:197]
	v_readfirstlane_b32 s0, v95
	s_mov_b32 m0, s0
	v_cvt_pk_f16_f32 v7, v6, v7
	global_load_lds_dwordx4 v[198:199], off
	v_cvt_pk_f16_f32 v6, v4, v5
	ds_write_b64 v100, v[6:7] offset:32768
	s_setprio 1
	s_waitcnt lgkmcnt(1)
	v_mfma_f32_16x16x32_f16 v[78:81], v[40:43], v[214:217], v[78:81]
	v_mfma_f32_16x16x32_f16 v[104:107], v[40:43], v[222:225], v[104:107]
	v_mfma_f32_16x16x32_f16 v[108:111], v[44:47], v[214:217], v[108:111]
	v_mfma_f32_16x16x32_f16 v[112:115], v[44:47], v[218:221], v[112:115]
	v_mfma_f32_16x16x32_f16 v[116:119], v[44:47], v[222:225], v[116:119]
	v_mfma_f32_16x16x32_f16 v[230:233], v[40:43], v[218:221], v[242:245]
	v_mfma_f32_16x16x32_f16 v[234:237], v[40:43], v[226:229], v[234:237]
	v_mfma_f32_16x16x32_f16 v[238:241], v[44:47], v[226:229], v[238:241]
	s_setprio 0
	ds_read_b128 v[44:47], v129 offset:4096
	ds_read_b128 v[242:245], v129 offset:6144
	v_readfirstlane_b32 s72, v96
	v_lshl_add_u64 v[40:41], v[198:199], 0, s[58:59]
	s_mov_b32 m0, s72
	s_nop 0
	global_load_lds_dwordx4 v[40:41], off
	v_cvt_pk_f16_f32 v41, v52, v53
	v_cvt_pk_f16_f32 v40, v50, v51
	ds_write_b64 v100, v[40:41] offset:36864
	s_add_u32 s70, s22, 0x20700
	s_addc_u32 s71, s90, 0
	s_add_u32 s100, s22, 0x700
	s_addc_u32 s101, s90, 0
	global_load_dwordx4 v[4:7], v201, s[100:101] nt
	s_setprio 1
	s_waitcnt lgkmcnt(1)
	v_mfma_f32_16x16x32_f16 v[82:85], v[44:47], v[214:217], v[82:85]
	v_mfma_f32_16x16x32_f16 v[120:123], v[44:47], v[226:229], v[120:123]
	v_mfma_f32_16x16x32_f16 v[124:127], v[242:245], v[214:217], v[124:127]
	v_mfma_f32_16x16x32_f16 v[146:149], v[242:245], v[218:221], v[146:149]
	v_mfma_f32_16x16x32_f16 v[134:137], v[242:245], v[226:229], v[134:137]
	v_mfma_f32_16x16x32_f16 v[138:141], v[44:47], v[218:221], v[138:141]
	v_mfma_f32_16x16x32_f16 v[142:145], v[44:47], v[222:225], v[142:145]
	v_mfma_f32_16x16x32_f16 v[150:153], v[242:245], v[222:225], v[150:153]
	s_setprio 0
	ds_read_b128 v[48:51], v129 offset:8192
	ds_read_b128 v[242:245], v129 offset:10240
	v_readfirstlane_b32 s71, v97
	v_lshl_add_u64 v[44:45], v[198:199], 0, s[60:61]
	s_mov_b32 m0, s71
	s_nop 0
	global_load_lds_dwordx4 v[44:45], off
	v_cvt_pk_f16_f32 v45, v56, v57
	v_cvt_pk_f16_f32 v44, v54, v55
	ds_write_b64 v100, v[44:45] offset:40960
	s_add_u32 s80, s22, 0x40700
	s_addc_u32 s81, s90, 0
	s_add_u32 s100, s22, 0x20700
	s_addc_u32 s101, s90, 0
	global_load_dwordx4 v[40:43], v201, s[100:101] nt
	s_setprio 1
	s_waitcnt lgkmcnt(1)
	v_mfma_f32_16x16x32_f16 v[86:89], v[48:51], v[214:217], v[86:89]
	v_mfma_f32_16x16x32_f16 v[170:173], v[48:51], v[218:221], v[170:173]
	v_mfma_f32_16x16x32_f16 v[174:177], v[48:51], v[222:225], v[174:177]
	v_mfma_f32_16x16x32_f16 v[162:165], v[48:51], v[226:229], v[162:165]
	v_mfma_f32_16x16x32_f16 v[178:181], v[242:245], v[214:217], v[178:181]
	v_mfma_f32_16x16x32_f16 v[182:185], v[242:245], v[218:221], v[182:185]
	v_mfma_f32_16x16x32_f16 v[186:189], v[242:245], v[222:225], v[186:189]
	v_mfma_f32_16x16x32_f16 v[154:157], v[242:245], v[226:229], v[154:157]
	s_setprio 0
	ds_read_b128 v[52:55], v129 offset:12288
	ds_read_b128 v[242:245], v129 offset:14336
	v_readfirstlane_b32 s70, v98
	v_lshl_add_u64 v[48:49], v[198:199], 0, s[62:63]
	s_mov_b32 m0, s70
	s_nop 0
	global_load_lds_dwordx4 v[48:49], off
	v_cvt_pk_f16_f32 v49, v60, v61
	v_cvt_pk_f16_f32 v48, v58, v59
	ds_write_b64 v100, v[48:49] offset:45056
	s_add_u32 s80, s22, 0x60700
	s_addc_u32 s81, s90, 0
	s_add_u32 s100, s22, 0x40700
	s_addc_u32 s101, s90, 0
	global_load_dwordx4 v[44:47], v201, s[100:101] nt
	s_setprio 1
	s_waitcnt lgkmcnt(1)
	v_mfma_f32_16x16x32_f16 v[74:77], v[52:55], v[214:217], v[74:77]
	v_mfma_f32_16x16x32_f16 v[90:93], v[52:55], v[218:221], v[90:93]
	v_mfma_f32_16x16x32_f16 v[158:161], v[52:55], v[222:225], v[158:161]
	v_mfma_f32_16x16x32_f16 v[166:169], v[52:55], v[226:229], v[166:169]
	v_mfma_f32_16x16x32_f16 v[190:193], v[242:245], v[214:217], v[190:193]
	v_mfma_f32_16x16x32_f16 v[202:205], v[242:245], v[218:221], v[202:205]
	v_mfma_f32_16x16x32_f16 v[206:209], v[242:245], v[222:225], v[206:209]
	v_mfma_f32_16x16x32_f16 v[210:213], v[242:245], v[226:229], v[210:213]
	s_setprio 0
	ds_read_b128 v[214:217], v128
	ds_read_b128 v[218:221], v128 offset:2048
	ds_read_b128 v[222:225], v128 offset:4096
	ds_read_b128 v[226:229], v128 offset:6144
	ds_read_b128 v[56:59], v130
	ds_read_b128 v[242:245], v130 offset:2048
	v_cvt_pk_f16_f32 v53, v64, v65
	v_cvt_pk_f16_f32 v52, v62, v63
	ds_write_b64 v100, v[52:53] offset:49152
	s_add_u32 s80, s22, 0x80700
	s_addc_u32 s81, s90, 0
	s_add_u32 s100, s22, 0x60700
	s_addc_u32 s101, s90, 0
	global_load_dwordx4 v[48:51], v201, s[100:101] nt
	s_add_u32 s100, s22, 0x80700
	s_addc_u32 s101, s90, 0
	global_load_dwordx4 v[52:55], v201, s[100:101] nt
	s_setprio 1
	s_waitcnt lgkmcnt(1)
	v_mfma_f32_16x16x32_f16 v[78:81], v[56:59], v[214:217], v[78:81]
	v_mfma_f32_16x16x32_f16 v[104:107], v[56:59], v[222:225], v[104:107]
	v_mfma_f32_16x16x32_f16 v[108:111], v[242:245], v[214:217], v[108:111]
	v_mfma_f32_16x16x32_f16 v[112:115], v[242:245], v[218:221], v[112:115]
	v_mfma_f32_16x16x32_f16 v[116:119], v[242:245], v[222:225], v[116:119]
	v_mfma_f32_16x16x32_f16 v[230:233], v[56:59], v[218:221], v[230:233]
	v_mfma_f32_16x16x32_f16 v[234:237], v[56:59], v[226:229], v[234:237]
	v_mfma_f32_16x16x32_f16 v[238:241], v[242:245], v[226:229], v[238:241]
	s_setprio 0
	ds_read_b128 v[60:63], v130 offset:4096
	ds_read_b128 v[242:245], v130 offset:6144
	v_cvt_pk_f16_f32 v57, v68, v69
	v_cvt_pk_f16_f32 v56, v66, v67
	ds_write_b64 v100, v[56:57] offset:53248
	s_add_u32 s80, s22, 0xa0700
	s_addc_u32 s81, s90, 0
	s_add_u32 s100, s22, 0xa0700
	s_addc_u32 s101, s90, 0
	global_load_dwordx4 v[56:59], v201, s[100:101] nt
	s_setprio 1
	s_waitcnt lgkmcnt(1)
	v_mfma_f32_16x16x32_f16 v[82:85], v[60:63], v[214:217], v[82:85]
	v_mfma_f32_16x16x32_f16 v[120:123], v[60:63], v[226:229], v[120:123]
	v_mfma_f32_16x16x32_f16 v[124:127], v[242:245], v[214:217], v[124:127]
	v_mfma_f32_16x16x32_f16 v[146:149], v[242:245], v[218:221], v[146:149]
	v_mfma_f32_16x16x32_f16 v[134:137], v[242:245], v[226:229], v[134:137]
	v_mfma_f32_16x16x32_f16 v[138:141], v[60:63], v[218:221], v[138:141]
	v_mfma_f32_16x16x32_f16 v[142:145], v[60:63], v[222:225], v[142:145]
	v_mfma_f32_16x16x32_f16 v[150:153], v[242:245], v[222:225], v[150:153]
	s_setprio 0
	ds_read_b128 v[64:67], v130 offset:8192
	ds_read_b128 v[242:245], v130 offset:10240
	v_cvt_pk_f16_f32 v61, v72, v73
	v_cvt_pk_f16_f32 v60, v70, v71
	ds_write_b64 v100, v[60:61] offset:57344
	s_add_u32 s80, s22, 0xc0700
	s_addc_u32 s81, s90, 0
	s_add_u32 s100, s22, 0xc0700
	s_addc_u32 s101, s90, 0
	global_load_dwordx4 v[60:63], v201, s[100:101] nt
	s_setprio 1
	s_waitcnt lgkmcnt(1)
	v_mfma_f32_16x16x32_f16 v[86:89], v[64:67], v[214:217], v[86:89]
	v_mfma_f32_16x16x32_f16 v[170:173], v[64:67], v[218:221], v[170:173]
	v_mfma_f32_16x16x32_f16 v[174:177], v[64:67], v[222:225], v[174:177]
	v_mfma_f32_16x16x32_f16 v[162:165], v[64:67], v[226:229], v[162:165]
	v_mfma_f32_16x16x32_f16 v[178:181], v[242:245], v[214:217], v[178:181]
	v_mfma_f32_16x16x32_f16 v[182:185], v[242:245], v[218:221], v[182:185]
	v_mfma_f32_16x16x32_f16 v[186:189], v[242:245], v[222:225], v[186:189]
	v_mfma_f32_16x16x32_f16 v[154:157], v[242:245], v[226:229], v[154:157]
	s_setprio 0
	ds_read_b128 v[64:67], v130 offset:12288
	ds_read_b128 v[68:71], v130 offset:14336
	v_cvt_pk_f16_f32 v39, v38, v39
	v_cvt_pk_f16_f32 v38, v36, v37
	ds_write_b64 v100, v[38:39] offset:61440
	s_add_u32 s80, s22, 0xe0700
	s_addc_u32 s81, s90, 0
	s_add_u32 s100, s22, 0xe0700
	s_addc_u32 s101, s90, 0
	global_load_dwordx4 v[36:39], v201, s[100:101] nt
	s_setprio 1
	s_waitcnt lgkmcnt(1)
	v_mfma_f32_16x16x32_f16 v[90:93], v[64:67], v[218:221], v[90:93]
	v_mfma_f32_16x16x32_f16 v[242:245], v[64:67], v[214:217], v[74:77]
	v_mfma_f32_16x16x32_f16 v[158:161], v[64:67], v[222:225], v[158:161]
	v_mfma_f32_16x16x32_f16 v[166:169], v[64:67], v[226:229], v[166:169]
	v_mfma_f32_16x16x32_f16 v[190:193], v[68:71], v[214:217], v[190:193]
	v_mfma_f32_16x16x32_f16 v[202:205], v[68:71], v[218:221], v[202:205]
	v_mfma_f32_16x16x32_f16 v[206:209], v[68:71], v[222:225], v[206:209]
	v_mfma_f32_16x16x32_f16 v[210:213], v[68:71], v[226:229], v[210:213]
	s_setprio 0
	s_waitcnt vmcnt(6)
	s_waitcnt lgkmcnt(0)
	s_barrier
	ds_read_b128 v[214:217], v131 offset:32768
	ds_read_b128 v[218:221], v131 offset:34816
	ds_read_b128 v[222:225], v131 offset:36864
	ds_read_b128 v[226:229], v131 offset:38912
	ds_read_b128 v[64:67], v129 offset:32768
	ds_read_b128 v[68:71], v129 offset:34816
	s_add_u32 s80, s22, 0x800
	s_addc_u32 s81, s90, 0
	v_lshl_add_u64 v[198:199], s[38:39], 0, v[196:197]
	v_readfirstlane_b32 s1, v94
	s_mov_b32 m0, s1
	v_cvt_pk_f16_f32 v3, v2, v3
	global_load_lds_dwordx4 v[198:199], off
	v_cvt_pk_f16_f32 v2, v0, v1
	ds_write_b64 v100, v[2:3]
	s_setprio 1
	s_waitcnt lgkmcnt(1)
	v_mfma_f32_16x16x32_f16 v[104:107], v[64:67], v[222:225], v[104:107]
	v_mfma_f32_16x16x32_f16 v[108:111], v[68:71], v[214:217], v[108:111]
	v_mfma_f32_16x16x32_f16 v[112:115], v[68:71], v[218:221], v[112:115]
	v_mfma_f32_16x16x32_f16 v[116:119], v[68:71], v[222:225], v[116:119]
	v_mfma_f32_16x16x32_f16 v[246:249], v[64:67], v[214:217], v[78:81]
	v_mfma_f32_16x16x32_f16 v[230:233], v[64:67], v[218:221], v[230:233]
	v_mfma_f32_16x16x32_f16 v[234:237], v[64:67], v[226:229], v[234:237]
	v_mfma_f32_16x16x32_f16 v[238:241], v[68:71], v[226:229], v[238:241]
	s_setprio 0
	ds_read_b128 v[68:71], v129 offset:36864
	ds_read_b128 v[72:75], v129 offset:38912
	v_readfirstlane_b32 s92, v99
	v_lshl_add_u64 v[64:65], v[198:199], 0, s[58:59]
	s_mov_b32 m0, s92
	v_cvt_pk_f16_f32 v11, v10, v11
	global_load_lds_dwordx4 v[64:65], off
	v_cvt_pk_f16_f32 v10, v8, v9
	ds_write_b64 v100, v[10:11] offset:4096
	s_add_u32 s80, s22, 0x20800
	s_addc_u32 s81, s90, 0
	s_add_u32 s100, s22, 0x800
	s_addc_u32 s101, s90, 0
	global_load_dwordx4 v[0:3], v201, s[100:101] nt
	s_setprio 1
	s_waitcnt lgkmcnt(1)
	v_mfma_f32_16x16x32_f16 v[8:11], v[68:71], v[214:217], v[82:85]
	v_mfma_f32_16x16x32_f16 v[120:123], v[68:71], v[226:229], v[120:123]
	v_mfma_f32_16x16x32_f16 v[124:127], v[72:75], v[214:217], v[124:127]
	v_mfma_f32_16x16x32_f16 v[146:149], v[72:75], v[218:221], v[146:149]
	v_mfma_f32_16x16x32_f16 v[134:137], v[72:75], v[226:229], v[134:137]
	v_mfma_f32_16x16x32_f16 v[138:141], v[68:71], v[218:221], v[138:141]
	v_mfma_f32_16x16x32_f16 v[142:145], v[68:71], v[222:225], v[142:145]
	v_mfma_f32_16x16x32_f16 v[150:153], v[72:75], v[222:225], v[150:153]
	s_setprio 0
	ds_read_b128 v[72:75], v129 offset:40960
	ds_read_b128 v[76:79], v129 offset:43008
	v_readfirstlane_b32 s91, v101
	v_lshl_add_u64 v[68:69], v[198:199], 0, s[60:61]
	s_mov_b32 m0, s91
	v_cvt_pk_f16_f32 v15, v14, v15
	global_load_lds_dwordx4 v[68:69], off
	v_cvt_pk_f16_f32 v14, v12, v13
	ds_write_b64 v100, v[14:15] offset:8192
	s_add_u32 s80, s22, 0x40800
	s_addc_u32 s81, s90, 0
	s_add_u32 s100, s22, 0x20800
	s_addc_u32 s101, s90, 0
	global_load_dwordx4 v[64:67], v201, s[100:101] nt
	s_setprio 1
	s_waitcnt lgkmcnt(1)
	v_mfma_f32_16x16x32_f16 v[12:15], v[72:75], v[214:217], v[86:89]
	v_mfma_f32_16x16x32_f16 v[170:173], v[72:75], v[218:221], v[170:173]
	v_mfma_f32_16x16x32_f16 v[174:177], v[72:75], v[222:225], v[174:177]
	v_mfma_f32_16x16x32_f16 v[162:165], v[72:75], v[226:229], v[162:165]
	v_mfma_f32_16x16x32_f16 v[178:181], v[76:79], v[214:217], v[178:181]
	v_mfma_f32_16x16x32_f16 v[182:185], v[76:79], v[218:221], v[182:185]
	v_mfma_f32_16x16x32_f16 v[186:189], v[76:79], v[222:225], v[186:189]
	v_mfma_f32_16x16x32_f16 v[154:157], v[76:79], v[226:229], v[154:157]
	s_setprio 0
	ds_read_b128 v[76:79], v129 offset:45056
	ds_read_b128 v[80:83], v129 offset:47104
	v_readfirstlane_b32 s73, v102
	v_lshl_add_u64 v[72:73], v[198:199], 0, s[62:63]
	s_mov_b32 m0, s73
	v_cvt_pk_f16_f32 v19, v18, v19
	global_load_lds_dwordx4 v[72:73], off
	v_cvt_pk_f16_f32 v18, v16, v17
	ds_write_b64 v100, v[18:19] offset:12288
	s_add_u32 s80, s22, 0x60800
	s_addc_u32 s81, s90, 0
	s_add_u32 s100, s22, 0x40800
	s_addc_u32 s101, s90, 0
	global_load_dwordx4 v[68:71], v201, s[100:101] nt
	s_setprio 1
	s_waitcnt lgkmcnt(1)
	v_mfma_f32_16x16x32_f16 v[16:19], v[76:79], v[214:217], v[242:245]
	v_mfma_f32_16x16x32_f16 v[242:245], v[76:79], v[218:221], v[90:93]
	v_mfma_f32_16x16x32_f16 v[158:161], v[76:79], v[222:225], v[158:161]
	v_mfma_f32_16x16x32_f16 v[166:169], v[76:79], v[226:229], v[166:169]
	v_mfma_f32_16x16x32_f16 v[190:193], v[80:83], v[214:217], v[190:193]
	v_mfma_f32_16x16x32_f16 v[202:205], v[80:83], v[218:221], v[202:205]
	v_mfma_f32_16x16x32_f16 v[206:209], v[80:83], v[222:225], v[206:209]
	v_mfma_f32_16x16x32_f16 v[210:213], v[80:83], v[226:229], v[210:213]
	s_setprio 0
	ds_read_b128 v[214:217], v128 offset:32768
	ds_read_b128 v[218:221], v128 offset:34816
	ds_read_b128 v[222:225], v128 offset:36864
	ds_read_b128 v[226:229], v128 offset:38912
	ds_read_b128 v[80:83], v130 offset:32768
	ds_read_b128 v[84:87], v130 offset:34816
	v_cvt_pk_f16_f32 v23, v22, v23
	v_cvt_pk_f16_f32 v22, v20, v21
	ds_write_b64 v100, v[22:23] offset:16384
	s_add_u32 s80, s22, 0x80800
	s_addc_u32 s81, s90, 0
	s_add_u32 s100, s22, 0x60800
	s_addc_u32 s101, s90, 0
	global_load_dwordx4 v[72:75], v201, s[100:101] nt
	s_add_u32 s100, s22, 0x80800
	s_addc_u32 s101, s90, 0
	global_load_dwordx4 v[76:79], v201, s[100:101] nt
	s_setprio 1
	s_waitcnt lgkmcnt(1)
	v_mfma_f32_16x16x32_f16 v[20:23], v[80:83], v[214:217], v[246:249]
	v_mfma_f32_16x16x32_f16 v[104:107], v[80:83], v[222:225], v[104:107]
	v_mfma_f32_16x16x32_f16 v[108:111], v[84:87], v[214:217], v[108:111]
	v_mfma_f32_16x16x32_f16 v[112:115], v[84:87], v[218:221], v[112:115]
	v_mfma_f32_16x16x32_f16 v[116:119], v[84:87], v[222:225], v[116:119]
	v_mfma_f32_16x16x32_f16 v[230:233], v[80:83], v[218:221], v[230:233]
	v_mfma_f32_16x16x32_f16 v[234:237], v[80:83], v[226:229], v[234:237]
	v_mfma_f32_16x16x32_f16 v[238:241], v[84:87], v[226:229], v[238:241]
	s_setprio 0
	ds_read_b128 v[84:87], v130 offset:36864
	ds_read_b128 v[88:91], v130 offset:38912
	v_cvt_pk_f16_f32 v27, v26, v27
	v_cvt_pk_f16_f32 v26, v24, v25
	ds_write_b64 v100, v[26:27] offset:20480
	s_add_u32 s80, s22, 0xa0800
	s_addc_u32 s81, s90, 0
	s_add_u32 s100, s22, 0xa0800
	s_addc_u32 s101, s90, 0
	global_load_dwordx4 v[80:83], v201, s[100:101] nt
	s_setprio 1
	s_waitcnt lgkmcnt(1)
	v_mfma_f32_16x16x32_f16 v[24:27], v[84:87], v[214:217], v[8:11]
	v_mfma_f32_16x16x32_f16 v[120:123], v[84:87], v[226:229], v[120:123]
	v_mfma_f32_16x16x32_f16 v[124:127], v[88:91], v[214:217], v[124:127]
	v_mfma_f32_16x16x32_f16 v[146:149], v[88:91], v[218:221], v[146:149]
	v_mfma_f32_16x16x32_f16 v[134:137], v[88:91], v[226:229], v[134:137]
	v_mfma_f32_16x16x32_f16 v[138:141], v[84:87], v[218:221], v[138:141]
	v_mfma_f32_16x16x32_f16 v[142:145], v[84:87], v[222:225], v[142:145]
	v_mfma_f32_16x16x32_f16 v[150:153], v[88:91], v[222:225], v[150:153]
	s_setprio 0
	ds_read_b128 v[8:11], v130 offset:40960
	ds_read_b128 v[88:91], v130 offset:43008
	v_cvt_pk_f16_f32 v31, v30, v31
	v_cvt_pk_f16_f32 v30, v28, v29
	ds_write_b64 v100, v[30:31] offset:24576
	s_add_u32 s80, s22, 0xc0800
	s_addc_u32 s81, s90, 0
	s_add_u32 s100, s22, 0xc0800
	s_addc_u32 s101, s90, 0
	global_load_dwordx4 v[84:87], v201, s[100:101] nt
	s_setprio 1
	s_waitcnt lgkmcnt(1)
	v_mfma_f32_16x16x32_f16 v[12:15], v[8:11], v[214:217], v[12:15]
	v_mfma_f32_16x16x32_f16 v[28:31], v[8:11], v[218:221], v[170:173]
	v_mfma_f32_16x16x32_f16 v[170:173], v[8:11], v[222:225], v[174:177]
	v_mfma_f32_16x16x32_f16 v[162:165], v[8:11], v[226:229], v[162:165]
	v_mfma_f32_16x16x32_f16 v[174:177], v[88:91], v[214:217], v[178:181]
	v_mfma_f32_16x16x32_f16 v[178:181], v[88:91], v[218:221], v[182:185]
	v_mfma_f32_16x16x32_f16 v[182:185], v[88:91], v[222:225], v[186:189]
	v_mfma_f32_16x16x32_f16 v[154:157], v[88:91], v[226:229], v[154:157]
	s_setprio 0
	ds_read_b128 v[8:11], v130 offset:45056
	ds_read_b128 v[186:189], v130 offset:47104
	v_cvt_pk_f16_f32 v35, v34, v35
	v_cvt_pk_f16_f32 v34, v32, v33
	ds_write_b64 v100, v[34:35] offset:28672
	s_add_u32 s80, s22, 0xe0800
	s_addc_u32 s81, s90, 0
	s_add_u32 s100, s22, 0xe0800
	s_addc_u32 s101, s90, 0
	global_load_dwordx4 v[88:91], v201, s[100:101] nt
	s_setprio 1
	s_waitcnt lgkmcnt(1)
	v_mfma_f32_16x16x32_f16 v[16:19], v[8:11], v[214:217], v[16:19]
	v_mfma_f32_16x16x32_f16 v[32:35], v[8:11], v[218:221], v[242:245]
	v_mfma_f32_16x16x32_f16 v[158:161], v[8:11], v[222:225], v[158:161]
	v_mfma_f32_16x16x32_f16 v[166:169], v[8:11], v[226:229], v[166:169]
	v_mfma_f32_16x16x32_f16 v[190:193], v[186:189], v[214:217], v[190:193]
	v_mfma_f32_16x16x32_f16 v[202:205], v[186:189], v[218:221], v[202:205]
	v_mfma_f32_16x16x32_f16 v[206:209], v[186:189], v[222:225], v[206:209]
	v_mfma_f32_16x16x32_f16 v[186:189], v[186:189], v[226:229], v[210:213]
	s_setprio 0
	s_waitcnt vmcnt(6)
	s_waitcnt lgkmcnt(0)
	s_barrier
	s_nop 0
	ds_read_b128 v[210:213], v131
	ds_read_b128 v[214:217], v131 offset:2048
	ds_read_b128 v[218:221], v131 offset:4096
	ds_read_b128 v[222:225], v131 offset:6144
	ds_read_b128 v[8:11], v129
	ds_read_b128 v[226:229], v129 offset:2048
	s_add_u32 s80, s22, 0x900
	v_lshl_add_u64 v[92:93], s[40:41], 0, v[196:197]
	s_addc_u32 s81, s90, 0
	v_cvt_pk_f16_f32 v7, v6, v7
	s_cmp_lg_u32 s2, 0
	s_cbranch_scc1 .Lres_skip_0
	s_add_u32 m0, s0, 0x18000
	s_nop 0
	global_load_lds_dwordx4 v[92:93], off

.Lres_skip_3:
	v_cvt_pk_f16_f32 v45, v50, v51
	v_cvt_pk_f16_f32 v44, v48, v49
	ds_write_b64 v100, v[44:45] offset:45056
	s_add_u32 s70, s22, 0x60900
	s_addc_u32 s71, s90, 0
	s_add_u32 s100, s22, 0x40900
	s_addc_u32 s101, s90, 0
	global_load_dwordx4 v[40:43], v201, s[100:101] nt
	s_setprio 1
	s_waitcnt lgkmcnt(1)
	v_mfma_f32_16x16x32_f16 v[16:19], v[238:241], v[210:213], v[16:19]
	v_mfma_f32_16x16x32_f16 v[32:35], v[238:241], v[214:217], v[32:35]
	v_mfma_f32_16x16x32_f16 v[158:161], v[238:241], v[218:221], v[158:161]
	v_mfma_f32_16x16x32_f16 v[166:169], v[238:241], v[222:225], v[166:169]
	v_mfma_f32_16x16x32_f16 v[190:193], v[242:245], v[210:213], v[190:193]
	v_mfma_f32_16x16x32_f16 v[202:205], v[242:245], v[214:217], v[202:205]
	v_mfma_f32_16x16x32_f16 v[206:209], v[242:245], v[218:221], v[206:209]
	v_mfma_f32_16x16x32_f16 v[186:189], v[242:245], v[222:225], v[186:189]
	s_setprio 0
	ds_read_b128 v[210:213], v128
	ds_read_b128 v[214:217], v128 offset:2048
	ds_read_b128 v[218:221], v128 offset:4096
	ds_read_b128 v[222:225], v128 offset:6144
	ds_read_b128 v[238:241], v130
	ds_read_b128 v[242:245], v130 offset:2048
	v_cvt_pk_f16_f32 v49, v54, v55
	v_cvt_pk_f16_f32 v48, v52, v53
	ds_write_b64 v100, v[48:49] offset:49152
	s_add_u32 s70, s22, 0x80900
	s_addc_u32 s71, s90, 0
	s_add_u32 s100, s22, 0x60900
	s_addc_u32 s101, s90, 0
	global_load_dwordx4 v[44:47], v201, s[100:101] nt
	s_add_u32 s100, s22, 0x80900
	s_addc_u32 s101, s90, 0
	global_load_dwordx4 v[48:51], v201, s[100:101] nt
	s_setprio 1
	s_waitcnt lgkmcnt(1)
	v_mfma_f32_16x16x32_f16 v[20:23], v[238:241], v[210:213], v[20:23]
	v_mfma_f32_16x16x32_f16 v[104:107], v[238:241], v[218:221], v[104:107]
	v_mfma_f32_16x16x32_f16 v[108:111], v[242:245], v[210:213], v[108:111]
	v_mfma_f32_16x16x32_f16 v[112:115], v[242:245], v[214:217], v[112:115]
	v_mfma_f32_16x16x32_f16 v[116:119], v[242:245], v[218:221], v[116:119]
	v_mfma_f32_16x16x32_f16 v[230:233], v[238:241], v[214:217], v[230:233]
	v_mfma_f32_16x16x32_f16 v[234:237], v[238:241], v[222:225], v[234:237]
	v_mfma_f32_16x16x32_f16 v[226:229], v[242:245], v[222:225], v[226:229]
	s_setprio 0
	ds_read_b128 v[238:241], v130 offset:4096
	ds_read_b128 v[242:245], v130 offset:6144
	v_cvt_pk_f16_f32 v53, v58, v59
	v_cvt_pk_f16_f32 v52, v56, v57
	ds_write_b64 v100, v[52:53] offset:53248
	s_add_u32 s70, s22, 0xa0900
	s_addc_u32 s71, s90, 0
	s_add_u32 s100, s22, 0xa0900
	s_addc_u32 s101, s90, 0
	global_load_dwordx4 v[52:55], v201, s[100:101] nt
	s_setprio 1
	s_waitcnt lgkmcnt(1)
	v_mfma_f32_16x16x32_f16 v[24:27], v[238:241], v[210:213], v[24:27]
	v_mfma_f32_16x16x32_f16 v[120:123], v[238:241], v[222:225], v[120:123]
	v_mfma_f32_16x16x32_f16 v[124:127], v[242:245], v[210:213], v[124:127]
	v_mfma_f32_16x16x32_f16 v[146:149], v[242:245], v[214:217], v[146:149]
	v_mfma_f32_16x16x32_f16 v[134:137], v[242:245], v[222:225], v[134:137]
	v_mfma_f32_16x16x32_f16 v[138:141], v[238:241], v[214:217], v[138:141]
	v_mfma_f32_16x16x32_f16 v[142:145], v[238:241], v[218:221], v[142:145]
	v_mfma_f32_16x16x32_f16 v[150:153], v[242:245], v[218:221], v[150:153]
	s_setprio 0
	ds_read_b128 v[238:241], v130 offset:8192
	ds_read_b128 v[242:245], v130 offset:10240
	v_cvt_pk_f16_f32 v57, v62, v63
	v_cvt_pk_f16_f32 v56, v60, v61
	ds_write_b64 v100, v[56:57] offset:57344
	s_add_u32 s70, s22, 0xc0900
	s_addc_u32 s71, s90, 0
	s_add_u32 s100, s22, 0xc0900
	s_addc_u32 s101, s90, 0
	global_load_dwordx4 v[56:59], v201, s[100:101] nt
	s_setprio 1
	s_waitcnt lgkmcnt(1)
	v_mfma_f32_16x16x32_f16 v[28:31], v[238:241], v[214:217], v[28:31]
	v_mfma_f32_16x16x32_f16 v[246:249], v[238:241], v[210:213], v[12:15]
	v_mfma_f32_16x16x32_f16 v[170:173], v[238:241], v[218:221], v[170:173]
	v_mfma_f32_16x16x32_f16 v[162:165], v[238:241], v[222:225], v[162:165]
	v_mfma_f32_16x16x32_f16 v[174:177], v[242:245], v[210:213], v[174:177]
	v_mfma_f32_16x16x32_f16 v[178:181], v[242:245], v[214:217], v[178:181]
	v_mfma_f32_16x16x32_f16 v[182:185], v[242:245], v[218:221], v[182:185]
	v_mfma_f32_16x16x32_f16 v[154:157], v[242:245], v[222:225], v[154:157]
	s_setprio 0
	ds_read_b128 v[12:15], v130 offset:12288
	ds_read_b128 v[238:241], v130 offset:14336
	v_cvt_pk_f16_f32 v39, v38, v39
	v_cvt_pk_f16_f32 v38, v36, v37
	ds_write_b64 v100, v[38:39] offset:61440
	s_add_u32 s70, s22, 0xe0900
	s_addc_u32 s71, s90, 0
	s_add_u32 s100, s22, 0xe0900
	s_addc_u32 s101, s90, 0
	global_load_dwordx4 v[60:63], v201, s[100:101] nt
	s_setprio 1
	s_waitcnt lgkmcnt(1)
	v_mfma_f32_16x16x32_f16 v[36:39], v[12:15], v[210:213], v[16:19]
	v_mfma_f32_16x16x32_f16 v[32:35], v[12:15], v[214:217], v[32:35]
	v_mfma_f32_16x16x32_f16 v[158:161], v[12:15], v[218:221], v[158:161]
	v_mfma_f32_16x16x32_f16 v[166:169], v[12:15], v[222:225], v[166:169]
	v_mfma_f32_16x16x32_f16 v[190:193], v[238:241], v[210:213], v[190:193]
	v_mfma_f32_16x16x32_f16 v[202:205], v[238:241], v[214:217], v[202:205]
	v_mfma_f32_16x16x32_f16 v[206:209], v[238:241], v[218:221], v[206:209]
	v_mfma_f32_16x16x32_f16 v[186:189], v[238:241], v[222:225], v[186:189]
	s_setprio 0
	s_waitcnt vmcnt(6)
	s_waitcnt lgkmcnt(0)
	s_barrier
	v_add_u32_e32 v250, 0x20000, v129
	v_add_u32_e32 v251, 0x20000, v130
	ds_read_b128 v[210:213], v131 offset:32768
	ds_read_b128 v[214:217], v131 offset:34816
	ds_read_b128 v[218:221], v131 offset:36864
	ds_read_b128 v[222:225], v131 offset:38912
	ds_read_b128 v[12:15], v250
	ds_read_b128 v[16:19], v250 offset:2048
	s_add_u32 s70, s22, 0xa00
	v_lshl_add_u64 v[92:93], s[42:43], 0, v[196:197]
	s_addc_u32 s71, s90, 0
	s_mov_b32 m0, s1
	v_cvt_pk_f16_f32 v3, v2, v3
	global_load_lds_dwordx4 v[92:93], off
	v_cvt_pk_f16_f32 v2, v0, v1
	ds_write_b64 v100, v[2:3]
	s_setprio 1
	s_waitcnt lgkmcnt(1)
	v_mfma_f32_16x16x32_f16 v[104:107], v[12:15], v[218:221], v[104:107]
	v_mfma_f32_16x16x32_f16 v[108:111], v[16:19], v[210:213], v[108:111]
	v_mfma_f32_16x16x32_f16 v[112:115], v[16:19], v[214:217], v[112:115]
	v_mfma_f32_16x16x32_f16 v[116:119], v[16:19], v[218:221], v[116:119]
	v_mfma_f32_16x16x32_f16 v[238:241], v[12:15], v[210:213], v[20:23]
	v_mfma_f32_16x16x32_f16 v[230:233], v[12:15], v[214:217], v[230:233]
	v_mfma_f32_16x16x32_f16 v[234:237], v[12:15], v[222:225], v[234:237]
	v_mfma_f32_16x16x32_f16 v[226:229], v[16:19], v[222:225], v[226:229]
	s_setprio 0
	ds_read_b128 v[16:19], v250 offset:4096
	ds_read_b128 v[20:23], v250 offset:6144
	s_mov_b32 m0, s92
	v_lshl_add_u64 v[12:13], v[92:93], 0, s[58:59]
	global_load_lds_dwordx4 v[12:13], off
	v_cvt_pk_f16_f32 v13, v66, v67
	v_cvt_pk_f16_f32 v12, v64, v65
	ds_write_b64 v100, v[12:13] offset:4096
	s_add_u32 s0, s22, 0x20a00
	s_addc_u32 s1, s90, 0
	s_add_u32 s100, s22, 0xa00
	s_addc_u32 s101, s90, 0
	global_load_dwordx4 v[0:3], v201, s[100:101] nt
	s_setprio 1
	s_waitcnt lgkmcnt(1)
	v_mfma_f32_16x16x32_f16 v[64:67], v[16:19], v[210:213], v[24:27]
	v_mfma_f32_16x16x32_f16 v[120:123], v[16:19], v[222:225], v[120:123]
	v_mfma_f32_16x16x32_f16 v[124:127], v[20:23], v[210:213], v[124:127]
	v_mfma_f32_16x16x32_f16 v[146:149], v[20:23], v[214:217], v[146:149]
	v_mfma_f32_16x16x32_f16 v[134:137], v[20:23], v[222:225], v[134:137]
	v_mfma_f32_16x16x32_f16 v[138:141], v[16:19], v[214:217], v[138:141]
	v_mfma_f32_16x16x32_f16 v[142:145], v[16:19], v[218:221], v[142:145]
	v_mfma_f32_16x16x32_f16 v[150:153], v[20:23], v[218:221], v[150:153]
	s_setprio 0
	ds_read_b128 v[20:23], v250 offset:8192
	ds_read_b128 v[24:27], v250 offset:10240
	s_mov_b32 m0, s91
	v_lshl_add_u64 v[16:17], v[92:93], 0, s[60:61]
	global_load_lds_dwordx4 v[16:17], off
	v_cvt_pk_f16_f32 v17, v70, v71
	v_cvt_pk_f16_f32 v16, v68, v69
	ds_write_b64 v100, v[16:17] offset:8192
	s_add_u32 s0, s22, 0x40a00
	s_addc_u32 s1, s90, 0
	s_add_u32 s100, s22, 0x20a00
	s_addc_u32 s101, s90, 0
	global_load_dwordx4 v[12:15], v201, s[100:101] nt
	s_setprio 1
	s_waitcnt lgkmcnt(1)
	v_mfma_f32_16x16x32_f16 v[68:71], v[20:23], v[210:213], v[246:249]
	v_mfma_f32_16x16x32_f16 v[242:245], v[20:23], v[214:217], v[28:31]
	v_mfma_f32_16x16x32_f16 v[170:173], v[20:23], v[218:221], v[170:173]
	v_mfma_f32_16x16x32_f16 v[162:165], v[20:23], v[222:225], v[162:165]
	v_mfma_f32_16x16x32_f16 v[174:177], v[24:27], v[210:213], v[174:177]
	v_mfma_f32_16x16x32_f16 v[178:181], v[24:27], v[214:217], v[178:181]
	v_mfma_f32_16x16x32_f16 v[182:185], v[24:27], v[218:221], v[182:185]
	v_mfma_f32_16x16x32_f16 v[154:157], v[24:27], v[222:225], v[154:157]
	s_setprio 0
	ds_read_b128 v[24:27], v250 offset:12288
	ds_read_b128 v[28:31], v250 offset:14336
	s_mov_b32 m0, s73
	v_lshl_add_u64 v[20:21], v[92:93], 0, s[62:63]
	global_load_lds_dwordx4 v[20:21], off
	v_cvt_pk_f16_f32 v21, v74, v75
	v_cvt_pk_f16_f32 v20, v72, v73
	ds_write_b64 v100, v[20:21] offset:12288
	s_add_u32 s0, s22, 0x60a00
	s_addc_u32 s1, s90, 0
	s_add_u32 s100, s22, 0x40a00
	s_addc_u32 s101, s90, 0
	global_load_dwordx4 v[16:19], v201, s[100:101] nt
	s_setprio 1
	s_waitcnt lgkmcnt(1)
	v_mfma_f32_16x16x32_f16 v[72:75], v[24:27], v[210:213], v[36:39]
	v_mfma_f32_16x16x32_f16 v[246:249], v[24:27], v[214:217], v[32:35]
	v_mfma_f32_16x16x32_f16 v[158:161], v[24:27], v[218:221], v[158:161]
	v_mfma_f32_16x16x32_f16 v[166:169], v[24:27], v[222:225], v[166:169]
	v_mfma_f32_16x16x32_f16 v[190:193], v[28:31], v[210:213], v[190:193]
	v_mfma_f32_16x16x32_f16 v[202:205], v[28:31], v[214:217], v[202:205]
	v_mfma_f32_16x16x32_f16 v[206:209], v[28:31], v[218:221], v[206:209]
	v_mfma_f32_16x16x32_f16 v[186:189], v[28:31], v[222:225], v[186:189]
	s_setprio 0
	ds_read_b128 v[210:213], v128 offset:32768
	ds_read_b128 v[214:217], v128 offset:34816
	ds_read_b128 v[218:221], v128 offset:36864
	ds_read_b128 v[222:225], v128 offset:38912
	ds_read_b128 v[28:31], v251
	ds_read_b128 v[32:35], v251 offset:2048
	v_cvt_pk_f16_f32 v25, v78, v79
	v_cvt_pk_f16_f32 v24, v76, v77
	ds_write_b64 v100, v[24:25] offset:16384
	s_add_u32 s0, s22, 0x80a00
	s_addc_u32 s1, s90, 0
	s_add_u32 s100, s22, 0x60a00
	s_addc_u32 s101, s90, 0
	global_load_dwordx4 v[20:23], v201, s[100:101] nt
	s_add_u32 s100, s22, 0x80a00
	s_addc_u32 s101, s90, 0
	global_load_dwordx4 v[24:27], v201, s[100:101] nt
	s_setprio 1
	s_waitcnt lgkmcnt(1)
	v_mfma_f32_16x16x32_f16 v[76:79], v[28:31], v[210:213], v[238:241]
	v_mfma_f32_16x16x32_f16 v[104:107], v[28:31], v[218:221], v[104:107]
	v_mfma_f32_16x16x32_f16 v[108:111], v[32:35], v[210:213], v[108:111]
	v_mfma_f32_16x16x32_f16 v[112:115], v[32:35], v[214:217], v[112:115]
	v_mfma_f32_16x16x32_f16 v[116:119], v[32:35], v[218:221], v[116:119]
	v_mfma_f32_16x16x32_f16 v[230:233], v[28:31], v[214:217], v[230:233]
	v_mfma_f32_16x16x32_f16 v[234:237], v[28:31], v[222:225], v[234:237]
	v_mfma_f32_16x16x32_f16 v[226:229], v[32:35], v[222:225], v[226:229]
	s_setprio 0
	ds_read_b128 v[32:35], v251 offset:4096
	ds_read_b128 v[36:39], v251 offset:6144
	v_cvt_pk_f16_f32 v29, v82, v83
	v_cvt_pk_f16_f32 v28, v80, v81
	ds_write_b64 v100, v[28:29] offset:20480
	s_add_u32 s0, s22, 0xa0a00
	s_addc_u32 s1, s90, 0
	s_add_u32 s100, s22, 0xa0a00
	s_addc_u32 s101, s90, 0
	global_load_dwordx4 v[28:31], v201, s[100:101] nt
	s_setprio 1
	s_waitcnt lgkmcnt(1)
	v_mfma_f32_16x16x32_f16 v[80:83], v[32:35], v[210:213], v[64:67]
	v_mfma_f32_16x16x32_f16 v[120:123], v[32:35], v[222:225], v[120:123]
	v_mfma_f32_16x16x32_f16 v[124:127], v[36:39], v[210:213], v[124:127]
	v_mfma_f32_16x16x32_f16 v[146:149], v[36:39], v[214:217], v[146:149]
	v_mfma_f32_16x16x32_f16 v[134:137], v[36:39], v[222:225], v[134:137]
	v_mfma_f32_16x16x32_f16 v[138:141], v[32:35], v[214:217], v[138:141]
	v_mfma_f32_16x16x32_f16 v[142:145], v[32:35], v[218:221], v[142:145]
	v_mfma_f32_16x16x32_f16 v[150:153], v[36:39], v[218:221], v[150:153]
	s_setprio 0
	ds_read_b128 v[36:39], v251 offset:8192
	ds_read_b128 v[64:67], v251 offset:10240
	v_cvt_pk_f16_f32 v33, v86, v87
	v_cvt_pk_f16_f32 v32, v84, v85
	ds_write_b64 v100, v[32:33] offset:24576
	s_add_u32 s0, s22, 0xc0a00
	s_addc_u32 s1, s90, 0
	s_add_u32 s100, s22, 0xc0a00
	s_addc_u32 s101, s90, 0
	global_load_dwordx4 v[32:35], v201, s[100:101] nt
	s_setprio 1
	s_waitcnt lgkmcnt(1)
	v_mfma_f32_16x16x32_f16 v[68:71], v[36:39], v[210:213], v[68:71]
	v_mfma_f32_16x16x32_f16 v[84:87], v[36:39], v[214:217], v[242:245]
	v_mfma_f32_16x16x32_f16 v[170:173], v[36:39], v[218:221], v[170:173]
	v_mfma_f32_16x16x32_f16 v[162:165], v[36:39], v[222:225], v[162:165]
	v_mfma_f32_16x16x32_f16 v[174:177], v[64:67], v[210:213], v[174:177]
	v_mfma_f32_16x16x32_f16 v[178:181], v[64:67], v[214:217], v[178:181]
	v_mfma_f32_16x16x32_f16 v[182:185], v[64:67], v[218:221], v[182:185]
	v_mfma_f32_16x16x32_f16 v[154:157], v[64:67], v[222:225], v[154:157]
	s_setprio 0
	ds_read_b128 v[64:67], v251 offset:12288
	ds_read_b128 v[238:241], v251 offset:14336
	v_cvt_pk_f16_f32 v37, v90, v91
	v_cvt_pk_f16_f32 v36, v88, v89
	ds_write_b64 v100, v[36:37] offset:28672
	s_add_u32 s0, s22, 0xe0a00
	s_addc_u32 s1, s90, 0
	s_add_u32 s100, s22, 0xe0a00
	s_addc_u32 s101, s90, 0
	global_load_dwordx4 v[36:39], v201, s[100:101] nt
	s_setprio 1
	s_waitcnt lgkmcnt(1)
	v_mfma_f32_16x16x32_f16 v[72:75], v[64:67], v[210:213], v[72:75]
	v_mfma_f32_16x16x32_f16 v[88:91], v[64:67], v[214:217], v[246:249]
	v_mfma_f32_16x16x32_f16 v[158:161], v[64:67], v[218:221], v[158:161]
	v_mfma_f32_16x16x32_f16 v[166:169], v[64:67], v[222:225], v[166:169]
	v_mfma_f32_16x16x32_f16 v[190:193], v[238:241], v[210:213], v[190:193]
	v_mfma_f32_16x16x32_f16 v[202:205], v[238:241], v[214:217], v[202:205]
	v_mfma_f32_16x16x32_f16 v[206:209], v[238:241], v[218:221], v[206:209]
	v_mfma_f32_16x16x32_f16 v[186:189], v[238:241], v[222:225], v[186:189]
	s_setprio 0
	s_waitcnt vmcnt(6)
	s_waitcnt lgkmcnt(0)
	s_barrier
	ds_read_b128 v[210:213], v131
	ds_read_b128 v[214:217], v131 offset:2048
	ds_read_b128 v[218:221], v131 offset:4096
	ds_read_b128 v[222:225], v131 offset:6144
	ds_read_b128 v[64:67], v129
	ds_read_b128 v[238:241], v129 offset:2048
	s_add_u32 s70, s22, 0xb00
	v_lshl_add_u64 v[92:93], s[44:45], 0, v[196:197]
	s_addc_u32 s71, s90, 0
	v_readfirstlane_b32 s0, v95
	s_mov_b32 m0, s0
	v_cvt_pk_f16_f32 v7, v6, v7
	global_load_lds_dwordx4 v[92:93], off
	v_cvt_pk_f16_f32 v6, v4, v5
	ds_write_b64 v100, v[6:7] offset:32768
	s_setprio 1
	s_waitcnt lgkmcnt(1)
	v_mfma_f32_16x16x32_f16 v[76:79], v[64:67], v[210:213], v[76:79]
	v_mfma_f32_16x16x32_f16 v[104:107], v[64:67], v[218:221], v[104:107]
	v_mfma_f32_16x16x32_f16 v[108:111], v[238:241], v[210:213], v[108:111]
	v_mfma_f32_16x16x32_f16 v[112:115], v[238:241], v[214:217], v[112:115]
	v_mfma_f32_16x16x32_f16 v[116:119], v[238:241], v[218:221], v[116:119]
	v_mfma_f32_16x16x32_f16 v[230:233], v[64:67], v[214:217], v[230:233]
	v_mfma_f32_16x16x32_f16 v[234:237], v[64:67], v[222:225], v[234:237]
	v_mfma_f32_16x16x32_f16 v[226:229], v[238:241], v[222:225], v[226:229]
	s_setprio 0
	ds_read_b128 v[238:241], v129 offset:4096
	ds_read_b128 v[242:245], v129 offset:6144
	v_readfirstlane_b32 s72, v96
	v_lshl_add_u64 v[64:65], v[92:93], 0, s[58:59]
	s_mov_b32 m0, s72
	v_cvt_pk_f16_f32 v11, v10, v11
	global_load_lds_dwordx4 v[64:65], off
	v_cvt_pk_f16_f32 v10, v8, v9
	ds_write_b64 v100, v[10:11] offset:36864
	s_add_u32 s70, s22, 0x20b00
	s_addc_u32 s71, s90, 0
	s_add_u32 s100, s22, 0xb00
	s_addc_u32 s101, s90, 0
	global_load_dwordx4 v[4:7], v201, s[100:101] nt
	s_setprio 1
	s_waitcnt lgkmcnt(1)
	v_mfma_f32_16x16x32_f16 v[8:11], v[238:241], v[210:213], v[80:83]
	v_mfma_f32_16x16x32_f16 v[80:83], v[238:241], v[214:217], v[138:141]
	v_mfma_f32_16x16x32_f16 v[138:141], v[238:241], v[218:221], v[142:145]
	v_mfma_f32_16x16x32_f16 v[120:123], v[238:241], v[222:225], v[120:123]
	v_mfma_f32_16x16x32_f16 v[124:127], v[242:245], v[210:213], v[124:127]
	v_mfma_f32_16x16x32_f16 v[142:145], v[242:245], v[214:217], v[146:149]
	v_mfma_f32_16x16x32_f16 v[146:149], v[242:245], v[218:221], v[150:153]
	v_mfma_f32_16x16x32_f16 v[134:137], v[242:245], v[222:225], v[134:137]
	s_setprio 0
	s_nop 0
	ds_read_b128 v[150:153], v129 offset:8192
	ds_read_b128 v[238:241], v129 offset:10240
	v_readfirstlane_b32 s71, v97
	v_lshl_add_u64 v[198:199], v[92:93], 0, s[60:61]
	s_mov_b32 m0, s71
	v_cvt_pk_f16_f32 v43, v42, v43
	global_load_lds_dwordx4 v[198:199], off
	v_cvt_pk_f16_f32 v42, v40, v41
	ds_write_b64 v100, v[42:43] offset:40960
	s_add_u32 s80, s22, 0x40b00
	s_addc_u32 s81, s90, 0
	s_add_u32 s100, s22, 0x20b00
	s_addc_u32 s101, s90, 0
	global_load_dwordx4 v[64:67], v201, s[100:101] nt
	s_setprio 1
	s_waitcnt lgkmcnt(1)
	v_mfma_f32_16x16x32_f16 v[68:71], v[150:153], v[210:213], v[68:71]
	v_mfma_f32_16x16x32_f16 v[84:87], v[150:153], v[214:217], v[84:87]
	v_mfma_f32_16x16x32_f16 v[170:173], v[150:153], v[218:221], v[170:173]
	v_mfma_f32_16x16x32_f16 v[150:153], v[150:153], v[222:225], v[162:165]
	v_mfma_f32_16x16x32_f16 v[162:165], v[238:241], v[210:213], v[174:177]
	v_mfma_f32_16x16x32_f16 v[174:177], v[238:241], v[214:217], v[178:181]
	v_mfma_f32_16x16x32_f16 v[178:181], v[238:241], v[218:221], v[182:185]
	v_mfma_f32_16x16x32_f16 v[154:157], v[238:241], v[222:225], v[154:157]
	s_setprio 0
	s_nop 0
	ds_read_b128 v[182:185], v129 offset:12288
	ds_read_b128 v[238:241], v129 offset:14336
	v_readfirstlane_b32 s70, v98
	v_lshl_add_u64 v[92:93], v[92:93], 0, s[62:63]
	s_mov_b32 m0, s70
	v_cvt_pk_f16_f32 v47, v46, v47
	global_load_lds_dwordx4 v[92:93], off
	v_cvt_pk_f16_f32 v46, v44, v45
	ds_write_b64 v100, v[46:47] offset:45056
	s_add_u32 s80, s22, 0x60b00
	s_addc_u32 s81, s90, 0
	s_add_u32 s100, s22, 0x40b00
	s_addc_u32 s101, s90, 0
	global_load_dwordx4 v[40:43], v201, s[100:101] nt
	s_setprio 1
	s_waitcnt lgkmcnt(1)
	v_mfma_f32_16x16x32_f16 v[72:75], v[182:185], v[210:213], v[72:75]
	v_mfma_f32_16x16x32_f16 v[88:91], v[182:185], v[214:217], v[88:91]
	v_mfma_f32_16x16x32_f16 v[158:161], v[182:185], v[218:221], v[158:161]
	v_mfma_f32_16x16x32_f16 v[166:169], v[182:185], v[222:225], v[166:169]
	v_mfma_f32_16x16x32_f16 v[182:185], v[238:241], v[210:213], v[190:193]
	v_mfma_f32_16x16x32_f16 v[190:193], v[238:241], v[214:217], v[202:205]
	v_mfma_f32_16x16x32_f16 v[202:205], v[238:241], v[218:221], v[206:209]
	v_mfma_f32_16x16x32_f16 v[186:189], v[238:241], v[222:225], v[186:189]
	s_setprio 0
	s_nop 0
	ds_read_b128 v[206:209], v128
	ds_read_b128 v[210:213], v128 offset:2048
	ds_read_b128 v[214:217], v128 offset:4096
	ds_read_b128 v[218:221], v128 offset:6144
	ds_read_b128 v[222:225], v130
	ds_read_b128 v[238:241], v130 offset:2048
	v_cvt_pk_f16_f32 v51, v50, v51
	v_cvt_pk_f16_f32 v50, v48, v49
	ds_write_b64 v100, v[50:51] offset:49152
	s_add_u32 s80, s22, 0x80b00
	s_addc_u32 s81, s90, 0
	s_add_u32 s100, s22, 0x60b00
	s_addc_u32 s101, s90, 0
	global_load_dwordx4 v[44:47], v201, s[100:101] nt
	s_add_u32 s100, s22, 0x80b00
	s_addc_u32 s101, s90, 0
	global_load_dwordx4 v[48:51], v201, s[100:101] nt
	s_setprio 1
	s_waitcnt lgkmcnt(1)
	v_mfma_f32_16x16x32_f16 v[76:79], v[222:225], v[206:209], v[76:79]
	v_mfma_f32_16x16x32_f16 v[104:107], v[222:225], v[214:217], v[104:107]
	v_mfma_f32_16x16x32_f16 v[108:111], v[238:241], v[206:209], v[108:111]
	v_mfma_f32_16x16x32_f16 v[112:115], v[238:241], v[210:213], v[112:115]
	v_mfma_f32_16x16x32_f16 v[116:119], v[238:241], v[214:217], v[116:119]
	v_mfma_f32_16x16x32_f16 v[230:233], v[222:225], v[210:213], v[230:233]
	v_mfma_f32_16x16x32_f16 v[222:225], v[222:225], v[218:221], v[234:237]
	v_mfma_f32_16x16x32_f16 v[226:229], v[238:241], v[218:221], v[226:229]
	s_setprio 0
	s_nop 0
	ds_read_b128 v[234:237], v130 offset:4096
	ds_read_b128 v[238:241], v130 offset:6144
	v_cvt_pk_f16_f32 v55, v54, v55
	v_cvt_pk_f16_f32 v54, v52, v53
	ds_write_b64 v100, v[54:55] offset:53248
	s_add_u32 s80, s22, 0xa0b00
	s_addc_u32 s81, s90, 0
	s_add_u32 s100, s22, 0xa0b00
	s_addc_u32 s101, s90, 0
	global_load_dwordx4 v[52:55], v201, s[100:101] nt
	s_setprio 1
	s_waitcnt lgkmcnt(1)
	v_mfma_f32_16x16x32_f16 v[80:83], v[234:237], v[210:213], v[80:83]
	v_mfma_f32_16x16x32_f16 v[120:123], v[234:237], v[218:221], v[120:123]
	v_mfma_f32_16x16x32_f16 v[124:127], v[238:241], v[206:209], v[124:127]
	v_mfma_f32_16x16x32_f16 v[146:149], v[238:241], v[214:217], v[146:149]
	v_mfma_f32_16x16x32_f16 v[134:137], v[238:241], v[218:221], v[134:137]
	v_mfma_f32_16x16x32_f16 v[242:245], v[234:237], v[206:209], v[8:11]
	v_mfma_f32_16x16x32_f16 v[138:141], v[234:237], v[214:217], v[138:141]
	v_mfma_f32_16x16x32_f16 v[142:145], v[238:241], v[210:213], v[142:145]
	s_setprio 0
	ds_read_b128 v[8:11], v130 offset:8192
	ds_read_b128 v[234:237], v130 offset:10240
	v_cvt_pk_f16_f32 v59, v58, v59
	v_cvt_pk_f16_f32 v58, v56, v57
	ds_write_b64 v100, v[58:59] offset:57344
	s_add_u32 s80, s22, 0xc0b00
	s_addc_u32 s81, s90, 0
	s_add_u32 s100, s22, 0xc0b00
	s_addc_u32 s101, s90, 0
	global_load_dwordx4 v[56:59], v201, s[100:101] nt
	s_setprio 1
	s_waitcnt lgkmcnt(1)
	v_mfma_f32_16x16x32_f16 v[84:87], v[8:11], v[210:213], v[84:87]
	v_mfma_f32_16x16x32_f16 v[238:241], v[8:11], v[206:209], v[68:71]
	v_mfma_f32_16x16x32_f16 v[170:173], v[8:11], v[214:217], v[170:173]
	v_mfma_f32_16x16x32_f16 v[150:153], v[8:11], v[218:221], v[150:153]
	v_mfma_f32_16x16x32_f16 v[162:165], v[234:237], v[206:209], v[162:165]
	v_mfma_f32_16x16x32_f16 v[174:177], v[234:237], v[210:213], v[174:177]
	v_mfma_f32_16x16x32_f16 v[178:181], v[234:237], v[214:217], v[178:181]
	v_mfma_f32_16x16x32_f16 v[154:157], v[234:237], v[218:221], v[154:157]
	s_setprio 0
	ds_read_b128 v[8:11], v130 offset:12288
	ds_read_b128 v[68:71], v130 offset:14336
	v_cvt_pk_f16_f32 v63, v62, v63
	v_cvt_pk_f16_f32 v62, v60, v61
	ds_write_b64 v100, v[62:63] offset:61440
	s_add_u32 s80, s22, 0xe0b00
	s_addc_u32 s81, s90, 0
	s_add_u32 s100, s22, 0xe0b00
	s_addc_u32 s101, s90, 0
	global_load_dwordx4 v[60:63], v201, s[100:101] nt
	s_setprio 1
	s_waitcnt lgkmcnt(1)
	v_mfma_f32_16x16x32_f16 v[88:91], v[8:11], v[210:213], v[88:91]
	v_mfma_f32_16x16x32_f16 v[234:237], v[8:11], v[206:209], v[72:75]
	v_mfma_f32_16x16x32_f16 v[158:161], v[8:11], v[214:217], v[158:161]
	v_mfma_f32_16x16x32_f16 v[166:169], v[8:11], v[218:221], v[166:169]
	v_mfma_f32_16x16x32_f16 v[182:185], v[68:71], v[206:209], v[182:185]
	v_mfma_f32_16x16x32_f16 v[190:193], v[68:71], v[210:213], v[190:193]
	v_mfma_f32_16x16x32_f16 v[202:205], v[68:71], v[214:217], v[202:205]
	v_mfma_f32_16x16x32_f16 v[186:189], v[68:71], v[218:221], v[186:189]
	s_setprio 0
	s_waitcnt vmcnt(6)
	s_waitcnt lgkmcnt(0)
	s_barrier
	ds_read_b128 v[206:209], v131 offset:32768
	ds_read_b128 v[210:213], v131 offset:34816
	ds_read_b128 v[214:217], v131 offset:36864
	ds_read_b128 v[218:221], v131 offset:38912
	ds_read_b128 v[68:71], v129 offset:32768
	ds_read_b128 v[72:75], v129 offset:34816
	s_add_u32 s80, s22, 0xc00
	v_lshl_add_u64 v[92:93], s[46:47], 0, v[196:197]
	s_addc_u32 s81, s90, 0
	v_readfirstlane_b32 s1, v94
	s_mov_b32 m0, s1
	v_cvt_pk_f16_f32 v3, v2, v3
	global_load_lds_dwordx4 v[92:93], off
	v_cvt_pk_f16_f32 v2, v0, v1
	ds_write_b64 v100, v[2:3]
	s_setprio 1
	s_waitcnt lgkmcnt(1)
	v_mfma_f32_16x16x32_f16 v[0:3], v[68:71], v[206:209], v[76:79]
	v_mfma_f32_16x16x32_f16 v[104:107], v[68:71], v[214:217], v[104:107]
	v_mfma_f32_16x16x32_f16 v[108:111], v[72:75], v[206:209], v[108:111]
	v_mfma_f32_16x16x32_f16 v[112:115], v[72:75], v[210:213], v[112:115]
	v_mfma_f32_16x16x32_f16 v[116:119], v[72:75], v[214:217], v[116:119]
	v_mfma_f32_16x16x32_f16 v[230:233], v[68:71], v[210:213], v[230:233]
	v_mfma_f32_16x16x32_f16 v[222:225], v[68:71], v[218:221], v[222:225]
	v_mfma_f32_16x16x32_f16 v[226:229], v[72:75], v[218:221], v[226:229]
	s_setprio 0
	ds_read_b128 v[72:75], v129 offset:36864
	ds_read_b128 v[76:79], v129 offset:38912
	v_readfirstlane_b32 s92, v99
	v_lshl_add_u64 v[68:69], v[92:93], 0, s[58:59]
	s_mov_b32 m0, s92
	v_cvt_pk_f16_f32 v15, v14, v15
	global_load_lds_dwordx4 v[68:69], off
	v_cvt_pk_f16_f32 v14, v12, v13
	ds_write_b64 v100, v[14:15] offset:4096
	s_add_u32 s80, s22, 0x20c00
	s_addc_u32 s81, s90, 0
	s_add_u32 s100, s22, 0xc00
	s_addc_u32 s101, s90, 0
	global_load_dwordx4 v[8:11], v201, s[100:101] nt
	s_setprio 1
	s_waitcnt lgkmcnt(1)
	v_mfma_f32_16x16x32_f16 v[12:15], v[72:75], v[206:209], v[242:245]
	v_mfma_f32_16x16x32_f16 v[120:123], v[72:75], v[218:221], v[120:123]
	v_mfma_f32_16x16x32_f16 v[124:127], v[76:79], v[206:209], v[124:127]
	v_mfma_f32_16x16x32_f16 v[146:149], v[76:79], v[214:217], v[146:149]
	v_mfma_f32_16x16x32_f16 v[134:137], v[76:79], v[218:221], v[134:137]
	v_mfma_f32_16x16x32_f16 v[242:245], v[72:75], v[210:213], v[80:83]
	v_mfma_f32_16x16x32_f16 v[138:141], v[72:75], v[214:217], v[138:141]
	v_mfma_f32_16x16x32_f16 v[142:145], v[76:79], v[210:213], v[142:145]
	s_setprio 0
	ds_read_b128 v[76:79], v129 offset:40960
	ds_read_b128 v[80:83], v129 offset:43008
	v_readfirstlane_b32 s91, v101
	v_lshl_add_u64 v[72:73], v[92:93], 0, s[60:61]
	s_mov_b32 m0, s91
	v_cvt_pk_f16_f32 v19, v18, v19
	global_load_lds_dwordx4 v[72:73], off
	v_cvt_pk_f16_f32 v18, v16, v17
	ds_write_b64 v100, v[18:19] offset:8192
	s_add_u32 s80, s22, 0x40c00
	s_addc_u32 s81, s90, 0
	s_add_u32 s100, s22, 0x20c00
	s_addc_u32 s101, s90, 0
	global_load_dwordx4 v[68:71], v201, s[100:101] nt
	s_setprio 1
	s_waitcnt lgkmcnt(1)
	v_mfma_f32_16x16x32_f16 v[16:19], v[76:79], v[206:209], v[238:241]
	v_mfma_f32_16x16x32_f16 v[238:241], v[76:79], v[210:213], v[84:87]
	v_mfma_f32_16x16x32_f16 v[170:173], v[76:79], v[214:217], v[170:173]
	v_mfma_f32_16x16x32_f16 v[150:153], v[76:79], v[218:221], v[150:153]
	v_mfma_f32_16x16x32_f16 v[162:165], v[80:83], v[206:209], v[162:165]
	v_mfma_f32_16x16x32_f16 v[174:177], v[80:83], v[210:213], v[174:177]
	v_mfma_f32_16x16x32_f16 v[178:181], v[80:83], v[214:217], v[178:181]
	v_mfma_f32_16x16x32_f16 v[154:157], v[80:83], v[218:221], v[154:157]
	s_setprio 0
	ds_read_b128 v[80:83], v129 offset:45056
	ds_read_b128 v[84:87], v129 offset:47104
	v_readfirstlane_b32 s73, v102
	v_lshl_add_u64 v[76:77], v[92:93], 0, s[62:63]
	s_mov_b32 m0, s73
	v_cvt_pk_f16_f32 v23, v22, v23
	global_load_lds_dwordx4 v[76:77], off
	v_cvt_pk_f16_f32 v22, v20, v21
	ds_write_b64 v100, v[22:23] offset:12288
	s_add_u32 s80, s22, 0x60c00
	s_addc_u32 s81, s90, 0
	s_add_u32 s100, s22, 0x40c00
	s_addc_u32 s101, s90, 0
	global_load_dwordx4 v[72:75], v201, s[100:101] nt
	s_setprio 1
	s_waitcnt lgkmcnt(1)
	v_mfma_f32_16x16x32_f16 v[20:23], v[80:83], v[206:209], v[234:237]
	v_mfma_f32_16x16x32_f16 v[234:237], v[80:83], v[210:213], v[88:91]
	v_mfma_f32_16x16x32_f16 v[158:161], v[80:83], v[214:217], v[158:161]
	v_mfma_f32_16x16x32_f16 v[166:169], v[80:83], v[218:221], v[166:169]
	v_mfma_f32_16x16x32_f16 v[182:185], v[84:87], v[206:209], v[182:185]
	v_mfma_f32_16x16x32_f16 v[190:193], v[84:87], v[210:213], v[190:193]
	v_mfma_f32_16x16x32_f16 v[202:205], v[84:87], v[214:217], v[202:205]
	v_mfma_f32_16x16x32_f16 v[186:189], v[84:87], v[218:221], v[186:189]
	s_setprio 0
	ds_read_b128 v[206:209], v128 offset:32768
	ds_read_b128 v[210:213], v128 offset:34816
	ds_read_b128 v[214:217], v128 offset:36864
	ds_read_b128 v[218:221], v128 offset:38912
	ds_read_b128 v[84:87], v130 offset:32768
	ds_read_b128 v[88:91], v130 offset:34816
	v_cvt_pk_f16_f32 v27, v26, v27
	v_cvt_pk_f16_f32 v26, v24, v25
	ds_write_b64 v100, v[26:27] offset:16384
	s_add_u32 s80, s22, 0x80c00
	s_addc_u32 s81, s90, 0
	s_add_u32 s100, s22, 0x60c00
	s_addc_u32 s101, s90, 0
	global_load_dwordx4 v[76:79], v201, s[100:101] nt
	s_add_u32 s100, s22, 0x80c00
	s_addc_u32 s101, s90, 0
	global_load_dwordx4 v[80:83], v201, s[100:101] nt
	s_setprio 1
	s_waitcnt lgkmcnt(1)
	v_mfma_f32_16x16x32_f16 v[24:27], v[84:87], v[206:209], v[0:3]
	v_mfma_f32_16x16x32_f16 v[104:107], v[84:87], v[214:217], v[104:107]
	v_mfma_f32_16x16x32_f16 v[108:111], v[88:91], v[206:209], v[108:111]
	v_mfma_f32_16x16x32_f16 v[112:115], v[88:91], v[210:213], v[112:115]
	v_mfma_f32_16x16x32_f16 v[116:119], v[88:91], v[214:217], v[116:119]
	v_mfma_f32_16x16x32_f16 v[230:233], v[84:87], v[210:213], v[230:233]
	v_mfma_f32_16x16x32_f16 v[222:225], v[84:87], v[218:221], v[222:225]
	v_mfma_f32_16x16x32_f16 v[226:229], v[88:91], v[218:221], v[226:229]
	s_setprio 0
	ds_read_b128 v[0:3], v130 offset:36864
	ds_read_b128 v[88:91], v130 offset:38912
	v_cvt_pk_f16_f32 v31, v30, v31
	v_cvt_pk_f16_f32 v30, v28, v29
	ds_write_b64 v100, v[30:31] offset:20480
	s_add_u32 s80, s22, 0xa0c00
	s_addc_u32 s81, s90, 0
	s_add_u32 s100, s22, 0xa0c00
	s_addc_u32 s101, s90, 0
	global_load_dwordx4 v[84:87], v201, s[100:101] nt
	s_setprio 1
	s_waitcnt lgkmcnt(1)
	v_mfma_f32_16x16x32_f16 v[12:15], v[0:3], v[206:209], v[12:15]
	v_mfma_f32_16x16x32_f16 v[28:31], v[0:3], v[210:213], v[242:245]
	v_mfma_f32_16x16x32_f16 v[120:123], v[0:3], v[218:221], v[120:123]
	v_mfma_f32_16x16x32_f16 v[124:127], v[88:91], v[206:209], v[124:127]
	v_mfma_f32_16x16x32_f16 v[146:149], v[88:91], v[214:217], v[146:149]
	v_mfma_f32_16x16x32_f16 v[134:137], v[88:91], v[218:221], v[134:137]
	v_mfma_f32_16x16x32_f16 v[138:141], v[0:3], v[214:217], v[138:141]
	v_mfma_f32_16x16x32_f16 v[142:145], v[88:91], v[210:213], v[142:145]
	s_setprio 0
	ds_read_b128 v[0:3], v130 offset:40960
	ds_read_b128 v[242:245], v130 offset:43008
	v_cvt_pk_f16_f32 v35, v34, v35
	v_cvt_pk_f16_f32 v34, v32, v33
	ds_write_b64 v100, v[34:35] offset:24576
	s_add_u32 s80, s22, 0xc0c00
	s_addc_u32 s81, s90, 0
	s_add_u32 s100, s22, 0xc0c00
	s_addc_u32 s101, s90, 0
	global_load_dwordx4 v[88:91], v201, s[100:101] nt
	s_setprio 1
	s_waitcnt lgkmcnt(1)
	v_mfma_f32_16x16x32_f16 v[16:19], v[0:3], v[206:209], v[16:19]
	v_mfma_f32_16x16x32_f16 v[32:35], v[0:3], v[210:213], v[238:241]
	v_mfma_f32_16x16x32_f16 v[170:173], v[0:3], v[214:217], v[170:173]
	v_mfma_f32_16x16x32_f16 v[150:153], v[0:3], v[218:221], v[150:153]
	v_mfma_f32_16x16x32_f16 v[162:165], v[242:245], v[206:209], v[162:165]
	v_mfma_f32_16x16x32_f16 v[174:177], v[242:245], v[210:213], v[174:177]
	v_mfma_f32_16x16x32_f16 v[178:181], v[242:245], v[214:217], v[178:181]
	v_mfma_f32_16x16x32_f16 v[154:157], v[242:245], v[218:221], v[154:157]
	s_setprio 0
	ds_read_b128 v[0:3], v130 offset:45056
	ds_read_b128 v[238:241], v130 offset:47104
	v_cvt_pk_f16_f32 v39, v38, v39
	v_cvt_pk_f16_f32 v38, v36, v37
	ds_write_b64 v100, v[38:39] offset:28672
	s_add_u32 s80, s22, 0xe0c00
	s_addc_u32 s81, s90, 0
	s_add_u32 s100, s22, 0xe0c00
	s_addc_u32 s101, s90, 0
	global_load_dwordx4 v[36:39], v201, s[100:101] nt
	s_setprio 1
	s_waitcnt lgkmcnt(1)
	v_mfma_f32_16x16x32_f16 v[20:23], v[0:3], v[206:209], v[20:23]
	v_mfma_f32_16x16x32_f16 v[234:237], v[0:3], v[210:213], v[234:237]
	v_mfma_f32_16x16x32_f16 v[158:161], v[0:3], v[214:217], v[158:161]
	v_mfma_f32_16x16x32_f16 v[166:169], v[0:3], v[218:221], v[166:169]
	v_mfma_f32_16x16x32_f16 v[182:185], v[238:241], v[206:209], v[182:185]
	v_mfma_f32_16x16x32_f16 v[190:193], v[238:241], v[210:213], v[190:193]
	v_mfma_f32_16x16x32_f16 v[202:205], v[238:241], v[214:217], v[202:205]
	v_mfma_f32_16x16x32_f16 v[186:189], v[238:241], v[218:221], v[186:189]
	s_setprio 0
	s_waitcnt vmcnt(6)
	s_waitcnt lgkmcnt(0)
	s_barrier
	ds_read_b128 v[206:209], v131
	ds_read_b128 v[210:213], v131 offset:2048
	ds_read_b128 v[214:217], v131 offset:4096
	ds_read_b128 v[218:221], v131 offset:6144
	ds_read_b128 v[238:241], v129
	ds_read_b128 v[242:245], v129 offset:2048
	s_add_u32 s80, s22, 0xd00
	v_lshl_add_u64 v[92:93], s[48:49], 0, v[196:197]
	s_addc_u32 s81, s90, 0
	s_mov_b32 m0, s0
	v_cvt_pk_f16_f32 v1, v6, v7
	global_load_lds_dwordx4 v[92:93], off
	v_cvt_pk_f16_f32 v0, v4, v5
	ds_write_b64 v100, v[0:1] offset:32768
	s_setprio 1
	s_waitcnt lgkmcnt(1)
	v_mfma_f32_16x16x32_f16 v[24:27], v[238:241], v[206:209], v[24:27]
	v_mfma_f32_16x16x32_f16 v[104:107], v[238:241], v[214:217], v[104:107]
	v_mfma_f32_16x16x32_f16 v[108:111], v[242:245], v[206:209], v[108:111]
	v_mfma_f32_16x16x32_f16 v[112:115], v[242:245], v[210:213], v[112:115]
	v_mfma_f32_16x16x32_f16 v[116:119], v[242:245], v[214:217], v[116:119]
	v_mfma_f32_16x16x32_f16 v[230:233], v[238:241], v[210:213], v[230:233]
	v_mfma_f32_16x16x32_f16 v[222:225], v[238:241], v[218:221], v[222:225]
	v_mfma_f32_16x16x32_f16 v[226:229], v[242:245], v[218:221], v[226:229]
	s_setprio 0
	ds_read_b128 v[238:241], v129 offset:4096
	ds_read_b128 v[242:245], v129 offset:6144
	s_mov_b32 m0, s72
	v_lshl_add_u64 v[4:5], v[92:93], 0, s[58:59]
	global_load_lds_dwordx4 v[4:5], off
	v_cvt_pk_f16_f32 v5, v66, v67
	v_cvt_pk_f16_f32 v4, v64, v65
	ds_write_b64 v100, v[4:5] offset:36864
	s_add_u32 s80, s22, 0x20d00
	s_addc_u32 s81, s90, 0
	s_add_u32 s100, s22, 0xd00
	s_addc_u32 s101, s90, 0
	global_load_dwordx4 v[0:3], v201, s[100:101] nt
	s_setprio 1
	s_waitcnt lgkmcnt(1)
	v_mfma_f32_16x16x32_f16 v[64:67], v[238:241], v[206:209], v[12:15]
	v_mfma_f32_16x16x32_f16 v[28:31], v[238:241], v[210:213], v[28:31]
	v_mfma_f32_16x16x32_f16 v[120:123], v[238:241], v[218:221], v[120:123]
	v_mfma_f32_16x16x32_f16 v[124:127], v[242:245], v[206:209], v[124:127]
	v_mfma_f32_16x16x32_f16 v[146:149], v[242:245], v[214:217], v[146:149]
	v_mfma_f32_16x16x32_f16 v[134:137], v[242:245], v[218:221], v[134:137]
	v_mfma_f32_16x16x32_f16 v[138:141], v[238:241], v[214:217], v[138:141]
	v_mfma_f32_16x16x32_f16 v[142:145], v[242:245], v[210:213], v[142:145]
	s_setprio 0
	ds_read_b128 v[238:241], v129 offset:8192
	ds_read_b128 v[242:245], v129 offset:10240
	s_mov_b32 m0, s71
	v_lshl_add_u64 v[12:13], v[92:93], 0, s[60:61]
	global_load_lds_dwordx4 v[12:13], off
	v_cvt_pk_f16_f32 v13, v42, v43
	v_cvt_pk_f16_f32 v12, v40, v41
	ds_write_b64 v100, v[12:13] offset:40960
	s_add_u32 s80, s22, 0x40d00
	s_addc_u32 s81, s90, 0
	s_add_u32 s100, s22, 0x20d00
	s_addc_u32 s101, s90, 0
	global_load_dwordx4 v[4:7], v201, s[100:101] nt
	s_setprio 1
	s_waitcnt lgkmcnt(1)
	v_mfma_f32_16x16x32_f16 v[40:43], v[238:241], v[206:209], v[16:19]
	v_mfma_f32_16x16x32_f16 v[32:35], v[238:241], v[210:213], v[32:35]
	v_mfma_f32_16x16x32_f16 v[170:173], v[238:241], v[214:217], v[170:173]
	v_mfma_f32_16x16x32_f16 v[150:153], v[238:241], v[218:221], v[150:153]
	v_mfma_f32_16x16x32_f16 v[162:165], v[242:245], v[206:209], v[162:165]
	v_mfma_f32_16x16x32_f16 v[174:177], v[242:245], v[210:213], v[174:177]
	v_mfma_f32_16x16x32_f16 v[178:181], v[242:245], v[214:217], v[178:181]
	v_mfma_f32_16x16x32_f16 v[154:157], v[242:245], v[218:221], v[154:157]
	s_setprio 0
	ds_read_b128 v[238:241], v129 offset:12288
	ds_read_b128 v[242:245], v129 offset:14336
	s_mov_b32 m0, s70
	v_lshl_add_u64 v[16:17], v[92:93], 0, s[62:63]
	global_load_lds_dwordx4 v[16:17], off
	v_cvt_pk_f16_f32 v17, v46, v47
	v_cvt_pk_f16_f32 v16, v44, v45
	ds_write_b64 v100, v[16:17] offset:45056
	s_add_u32 s70, s22, 0x60d00
	s_addc_u32 s71, s90, 0
	s_add_u32 s100, s22, 0x40d00
	s_addc_u32 s101, s90, 0
	global_load_dwordx4 v[12:15], v201, s[100:101] nt
	s_setprio 1
	s_waitcnt lgkmcnt(1)
	v_mfma_f32_16x16x32_f16 v[44:47], v[238:241], v[206:209], v[20:23]
	v_mfma_f32_16x16x32_f16 v[234:237], v[238:241], v[210:213], v[234:237]
	v_mfma_f32_16x16x32_f16 v[158:161], v[238:241], v[214:217], v[158:161]
	v_mfma_f32_16x16x32_f16 v[166:169], v[238:241], v[218:221], v[166:169]
	v_mfma_f32_16x16x32_f16 v[182:185], v[242:245], v[206:209], v[182:185]
	v_mfma_f32_16x16x32_f16 v[190:193], v[242:245], v[210:213], v[190:193]
	v_mfma_f32_16x16x32_f16 v[202:205], v[242:245], v[214:217], v[202:205]
	v_mfma_f32_16x16x32_f16 v[186:189], v[242:245], v[218:221], v[186:189]
	s_setprio 0
	ds_read_b128 v[206:209], v128
	ds_read_b128 v[210:213], v128 offset:2048
	ds_read_b128 v[214:217], v128 offset:4096
	ds_read_b128 v[218:221], v128 offset:6144
	ds_read_b128 v[238:241], v130
	ds_read_b128 v[242:245], v130 offset:2048
	v_cvt_pk_f16_f32 v21, v50, v51
	v_cvt_pk_f16_f32 v20, v48, v49
	ds_write_b64 v100, v[20:21] offset:49152
	s_add_u32 s70, s22, 0x80d00
	s_addc_u32 s71, s90, 0
	s_add_u32 s100, s22, 0x60d00
	s_addc_u32 s101, s90, 0
	global_load_dwordx4 v[16:19], v201, s[100:101] nt
	s_add_u32 s100, s22, 0x80d00
	s_addc_u32 s101, s90, 0
	global_load_dwordx4 v[20:23], v201, s[100:101] nt
	s_setprio 1
	s_waitcnt lgkmcnt(1)
	v_mfma_f32_16x16x32_f16 v[48:51], v[238:241], v[206:209], v[24:27]
	v_mfma_f32_16x16x32_f16 v[104:107], v[238:241], v[214:217], v[104:107]
	v_mfma_f32_16x16x32_f16 v[108:111], v[242:245], v[206:209], v[108:111]
	v_mfma_f32_16x16x32_f16 v[112:115], v[242:245], v[210:213], v[112:115]
	v_mfma_f32_16x16x32_f16 v[116:119], v[242:245], v[214:217], v[116:119]
	v_mfma_f32_16x16x32_f16 v[230:233], v[238:241], v[210:213], v[230:233]
	v_mfma_f32_16x16x32_f16 v[222:225], v[238:241], v[218:221], v[222:225]
	v_mfma_f32_16x16x32_f16 v[226:229], v[242:245], v[218:221], v[226:229]
	s_setprio 0
	ds_read_b128 v[238:241], v130 offset:4096
	ds_read_b128 v[242:245], v130 offset:6144
	v_cvt_pk_f16_f32 v25, v54, v55
	v_cvt_pk_f16_f32 v24, v52, v53
	ds_write_b64 v100, v[24:25] offset:53248
	s_add_u32 s70, s22, 0xa0d00
	s_addc_u32 s71, s90, 0
	s_add_u32 s100, s22, 0xa0d00
	s_addc_u32 s101, s90, 0
	global_load_dwordx4 v[24:27], v201, s[100:101] nt
	s_setprio 1
	s_waitcnt lgkmcnt(1)
	v_mfma_f32_16x16x32_f16 v[52:55], v[238:241], v[206:209], v[64:67]
	v_mfma_f32_16x16x32_f16 v[64:67], v[238:241], v[210:213], v[28:31]
	v_mfma_f32_16x16x32_f16 v[120:123], v[238:241], v[218:221], v[120:123]
	v_mfma_f32_16x16x32_f16 v[124:127], v[242:245], v[206:209], v[124:127]
	v_mfma_f32_16x16x32_f16 v[146:149], v[242:245], v[214:217], v[146:149]
	v_mfma_f32_16x16x32_f16 v[134:137], v[242:245], v[218:221], v[134:137]
	v_mfma_f32_16x16x32_f16 v[138:141], v[238:241], v[214:217], v[138:141]
	v_mfma_f32_16x16x32_f16 v[142:145], v[242:245], v[210:213], v[142:145]
	s_setprio 0
	ds_read_b128 v[238:241], v130 offset:8192
	ds_read_b128 v[242:245], v130 offset:10240
	v_cvt_pk_f16_f32 v29, v58, v59
	v_cvt_pk_f16_f32 v28, v56, v57
	ds_write_b64 v100, v[28:29] offset:57344
	s_add_u32 s70, s22, 0xc0d00
	s_addc_u32 s71, s90, 0
	s_add_u32 s100, s22, 0xc0d00
	s_addc_u32 s101, s90, 0
	global_load_dwordx4 v[28:31], v201, s[100:101] nt
	s_setprio 1
	s_waitcnt lgkmcnt(1)
	v_mfma_f32_16x16x32_f16 v[56:59], v[238:241], v[206:209], v[40:43]
	v_mfma_f32_16x16x32_f16 v[246:249], v[238:241], v[210:213], v[32:35]
	v_mfma_f32_16x16x32_f16 v[170:173], v[238:241], v[214:217], v[170:173]
	v_mfma_f32_16x16x32_f16 v[150:153], v[238:241], v[218:221], v[150:153]
	v_mfma_f32_16x16x32_f16 v[162:165], v[242:245], v[206:209], v[162:165]
	v_mfma_f32_16x16x32_f16 v[174:177], v[242:245], v[210:213], v[174:177]
	v_mfma_f32_16x16x32_f16 v[178:181], v[242:245], v[214:217], v[178:181]
	v_mfma_f32_16x16x32_f16 v[154:157], v[242:245], v[218:221], v[154:157]
	s_setprio 0
	ds_read_b128 v[40:43], v130 offset:12288
	ds_read_b128 v[238:241], v130 offset:14336
	v_cvt_pk_f16_f32 v33, v62, v63
	v_cvt_pk_f16_f32 v32, v60, v61
	ds_write_b64 v100, v[32:33] offset:61440
	s_add_u32 s70, s22, 0xe0d00
	s_addc_u32 s71, s90, 0
	s_add_u32 s100, s22, 0xe0d00
	s_addc_u32 s101, s90, 0
	global_load_dwordx4 v[32:35], v201, s[100:101] nt
	s_setprio 1
	s_waitcnt lgkmcnt(1)
	v_mfma_f32_16x16x32_f16 v[60:63], v[40:43], v[206:209], v[44:47]
	v_mfma_f32_16x16x32_f16 v[234:237], v[40:43], v[210:213], v[234:237]
	v_mfma_f32_16x16x32_f16 v[158:161], v[40:43], v[214:217], v[158:161]
	v_mfma_f32_16x16x32_f16 v[166:169], v[40:43], v[218:221], v[166:169]
	v_mfma_f32_16x16x32_f16 v[182:185], v[238:241], v[206:209], v[182:185]
	v_mfma_f32_16x16x32_f16 v[190:193], v[238:241], v[210:213], v[190:193]
	v_mfma_f32_16x16x32_f16 v[202:205], v[238:241], v[214:217], v[202:205]
	v_mfma_f32_16x16x32_f16 v[186:189], v[238:241], v[218:221], v[186:189]
	s_setprio 0
	s_waitcnt vmcnt(6)
	s_waitcnt lgkmcnt(0)
	s_barrier
	ds_read_b128 v[206:209], v131 offset:32768
	ds_read_b128 v[210:213], v131 offset:34816
	ds_read_b128 v[214:217], v131 offset:36864
	ds_read_b128 v[218:221], v131 offset:38912
	ds_read_b128 v[40:43], v129 offset:32768
	ds_read_b128 v[44:47], v129 offset:34816
	s_add_u32 s70, s22, 0xe00
	v_lshl_add_u64 v[92:93], s[50:51], 0, v[196:197]
	s_addc_u32 s71, s90, 0
	s_mov_b32 m0, s1
	v_cvt_pk_f16_f32 v11, v10, v11
	global_load_lds_dwordx4 v[92:93], off
	v_cvt_pk_f16_f32 v10, v8, v9
	ds_write_b64 v100, v[10:11]
	s_setprio 1
	s_waitcnt lgkmcnt(1)
	v_mfma_f32_16x16x32_f16 v[104:107], v[40:43], v[214:217], v[104:107]
	v_mfma_f32_16x16x32_f16 v[108:111], v[44:47], v[206:209], v[108:111]
	v_mfma_f32_16x16x32_f16 v[112:115], v[44:47], v[210:213], v[112:115]
	v_mfma_f32_16x16x32_f16 v[116:119], v[44:47], v[214:217], v[116:119]
	v_mfma_f32_16x16x32_f16 v[238:241], v[40:43], v[206:209], v[48:51]
	v_mfma_f32_16x16x32_f16 v[230:233], v[40:43], v[210:213], v[230:233]
	v_mfma_f32_16x16x32_f16 v[222:225], v[40:43], v[218:221], v[222:225]
	v_mfma_f32_16x16x32_f16 v[226:229], v[44:47], v[218:221], v[226:229]
	s_setprio 0
	ds_read_b128 v[44:47], v129 offset:36864
	ds_read_b128 v[48:51], v129 offset:38912
	s_mov_b32 m0, s92
	v_lshl_add_u64 v[40:41], v[92:93], 0, s[58:59]
	global_load_lds_dwordx4 v[40:41], off
	v_cvt_pk_f16_f32 v41, v70, v71
	v_cvt_pk_f16_f32 v40, v68, v69
	ds_write_b64 v100, v[40:41] offset:4096
	s_add_u32 s0, s22, 0x20e00
	s_addc_u32 s1, s90, 0
	s_add_u32 s100, s22, 0xe00
	s_addc_u32 s101, s90, 0
	global_load_dwordx4 v[8:11], v201, s[100:101] nt
	s_setprio 1
	s_waitcnt lgkmcnt(1)
	v_mfma_f32_16x16x32_f16 v[68:71], v[44:47], v[206:209], v[52:55]
	v_mfma_f32_16x16x32_f16 v[64:67], v[44:47], v[210:213], v[64:67]
	v_mfma_f32_16x16x32_f16 v[120:123], v[44:47], v[218:221], v[120:123]
	v_mfma_f32_16x16x32_f16 v[124:127], v[48:51], v[206:209], v[124:127]
	v_mfma_f32_16x16x32_f16 v[146:149], v[48:51], v[214:217], v[146:149]
	v_mfma_f32_16x16x32_f16 v[134:137], v[48:51], v[218:221], v[134:137]
	v_mfma_f32_16x16x32_f16 v[138:141], v[44:47], v[214:217], v[138:141]
	v_mfma_f32_16x16x32_f16 v[142:145], v[48:51], v[210:213], v[142:145]
	s_setprio 0
	ds_read_b128 v[48:51], v129 offset:40960
	ds_read_b128 v[52:55], v129 offset:43008
	s_mov_b32 m0, s91
	v_lshl_add_u64 v[44:45], v[92:93], 0, s[60:61]
	global_load_lds_dwordx4 v[44:45], off
	v_cvt_pk_f16_f32 v45, v74, v75
	v_cvt_pk_f16_f32 v44, v72, v73
	ds_write_b64 v100, v[44:45] offset:8192
	s_add_u32 s0, s22, 0x40e00
	s_addc_u32 s1, s90, 0
	s_add_u32 s100, s22, 0x20e00
	s_addc_u32 s101, s90, 0
	global_load_dwordx4 v[40:43], v201, s[100:101] nt
	s_setprio 1
	s_waitcnt lgkmcnt(1)
	v_mfma_f32_16x16x32_f16 v[72:75], v[48:51], v[206:209], v[56:59]
	v_mfma_f32_16x16x32_f16 v[242:245], v[48:51], v[210:213], v[246:249]
	v_mfma_f32_16x16x32_f16 v[170:173], v[48:51], v[214:217], v[170:173]
	v_mfma_f32_16x16x32_f16 v[150:153], v[48:51], v[218:221], v[150:153]
	v_mfma_f32_16x16x32_f16 v[162:165], v[52:55], v[206:209], v[162:165]
	v_mfma_f32_16x16x32_f16 v[174:177], v[52:55], v[210:213], v[174:177]
	v_mfma_f32_16x16x32_f16 v[178:181], v[52:55], v[214:217], v[178:181]
	v_mfma_f32_16x16x32_f16 v[154:157], v[52:55], v[218:221], v[154:157]
	s_setprio 0
	ds_read_b128 v[52:55], v129 offset:45056
	ds_read_b128 v[56:59], v129 offset:47104
	s_mov_b32 m0, s73
	v_lshl_add_u64 v[48:49], v[92:93], 0, s[62:63]
	global_load_lds_dwordx4 v[48:49], off
	v_cvt_pk_f16_f32 v49, v78, v79
	v_cvt_pk_f16_f32 v48, v76, v77
	ds_write_b64 v100, v[48:49] offset:12288
	s_add_u32 s0, s22, 0x60e00
	s_addc_u32 s1, s90, 0
	s_add_u32 s100, s22, 0x40e00
	s_addc_u32 s101, s90, 0
	global_load_dwordx4 v[44:47], v201, s[100:101] nt
	s_setprio 1
	s_waitcnt lgkmcnt(1)
	v_mfma_f32_16x16x32_f16 v[76:79], v[52:55], v[206:209], v[60:63]
	v_mfma_f32_16x16x32_f16 v[234:237], v[52:55], v[210:213], v[234:237]
	v_mfma_f32_16x16x32_f16 v[158:161], v[52:55], v[214:217], v[158:161]
	v_mfma_f32_16x16x32_f16 v[166:169], v[52:55], v[218:221], v[166:169]
	v_mfma_f32_16x16x32_f16 v[182:185], v[56:59], v[206:209], v[182:185]
	v_mfma_f32_16x16x32_f16 v[190:193], v[56:59], v[210:213], v[190:193]
	v_mfma_f32_16x16x32_f16 v[202:205], v[56:59], v[214:217], v[202:205]
	v_mfma_f32_16x16x32_f16 v[186:189], v[56:59], v[218:221], v[186:189]
	s_setprio 0
	ds_read_b128 v[206:209], v128 offset:32768
	ds_read_b128 v[210:213], v128 offset:34816
	ds_read_b128 v[214:217], v128 offset:36864
	ds_read_b128 v[218:221], v128 offset:38912
	ds_read_b128 v[56:59], v130 offset:32768
	ds_read_b128 v[60:63], v130 offset:34816
	v_cvt_pk_f16_f32 v53, v82, v83
	v_cvt_pk_f16_f32 v52, v80, v81
	ds_write_b64 v100, v[52:53] offset:16384
	s_add_u32 s0, s22, 0x80e00
	s_addc_u32 s1, s90, 0
	s_add_u32 s100, s22, 0x60e00
	s_addc_u32 s101, s90, 0
	global_load_dwordx4 v[48:51], v201, s[100:101] nt
	s_add_u32 s100, s22, 0x80e00
	s_addc_u32 s101, s90, 0
	global_load_dwordx4 v[52:55], v201, s[100:101] nt
	s_setprio 1
	s_waitcnt lgkmcnt(1)
	v_mfma_f32_16x16x32_f16 v[80:83], v[56:59], v[206:209], v[238:241]
	v_mfma_f32_16x16x32_f16 v[104:107], v[56:59], v[214:217], v[104:107]
	v_mfma_f32_16x16x32_f16 v[108:111], v[60:63], v[206:209], v[108:111]
	v_mfma_f32_16x16x32_f16 v[112:115], v[60:63], v[210:213], v[112:115]
	v_mfma_f32_16x16x32_f16 v[116:119], v[60:63], v[214:217], v[116:119]
	v_mfma_f32_16x16x32_f16 v[230:233], v[56:59], v[210:213], v[230:233]
	v_mfma_f32_16x16x32_f16 v[222:225], v[56:59], v[218:221], v[222:225]
	v_mfma_f32_16x16x32_f16 v[226:229], v[60:63], v[218:221], v[226:229]
	s_setprio 0
	ds_read_b128 v[60:63], v130 offset:36864
	ds_read_b128 v[238:241], v130 offset:38912
	v_cvt_pk_f16_f32 v57, v86, v87
	v_cvt_pk_f16_f32 v56, v84, v85
	ds_write_b64 v100, v[56:57] offset:20480
	s_add_u32 s0, s22, 0xa0e00
	s_addc_u32 s1, s90, 0
	s_add_u32 s100, s22, 0xa0e00
	s_addc_u32 s101, s90, 0
	global_load_dwordx4 v[56:59], v201, s[100:101] nt
	s_setprio 1
	s_waitcnt lgkmcnt(1)
	v_mfma_f32_16x16x32_f16 v[68:71], v[60:63], v[206:209], v[68:71]
	v_mfma_f32_16x16x32_f16 v[64:67], v[60:63], v[210:213], v[64:67]
	v_mfma_f32_16x16x32_f16 v[84:87], v[60:63], v[214:217], v[138:141]
	v_mfma_f32_16x16x32_f16 v[120:123], v[60:63], v[218:221], v[120:123]
	v_mfma_f32_16x16x32_f16 v[124:127], v[238:241], v[206:209], v[124:127]
	v_mfma_f32_16x16x32_f16 v[134:137], v[238:241], v[218:221], v[134:137]
	v_mfma_f32_16x16x32_f16 v[138:141], v[238:241], v[210:213], v[142:145]
	v_mfma_f32_16x16x32_f16 v[142:145], v[238:241], v[214:217], v[146:149]
	s_setprio 0
	s_nop 1
	ds_read_b128 v[146:149], v130 offset:40960
	ds_read_b128 v[238:241], v130 offset:43008
	v_cvt_pk_f16_f32 v61, v90, v91
	v_cvt_pk_f16_f32 v60, v88, v89
	ds_write_b64 v100, v[60:61] offset:24576
	s_add_u32 s0, s22, 0xc0e00
	s_addc_u32 s1, s90, 0
	s_add_u32 s100, s22, 0xc0e00
	s_addc_u32 s101, s90, 0
	global_load_dwordx4 v[60:63], v201, s[100:101] nt
	s_setprio 1
	s_waitcnt lgkmcnt(1)
	v_mfma_f32_16x16x32_f16 v[72:75], v[146:149], v[206:209], v[72:75]
	v_mfma_f32_16x16x32_f16 v[88:91], v[146:149], v[210:213], v[242:245]
	v_mfma_f32_16x16x32_f16 v[170:173], v[146:149], v[214:217], v[170:173]
	v_mfma_f32_16x16x32_f16 v[146:149], v[146:149], v[218:221], v[150:153]
	v_mfma_f32_16x16x32_f16 v[150:153], v[238:241], v[206:209], v[162:165]
	v_mfma_f32_16x16x32_f16 v[162:165], v[238:241], v[210:213], v[174:177]
	v_mfma_f32_16x16x32_f16 v[174:177], v[238:241], v[214:217], v[178:181]
	v_mfma_f32_16x16x32_f16 v[154:157], v[238:241], v[218:221], v[154:157]
	s_setprio 0
	s_nop 0
	ds_read_b128 v[178:181], v130 offset:45056
	ds_read_b128 v[238:241], v130 offset:47104
	v_cvt_pk_f16_f32 v39, v38, v39
	v_cvt_pk_f16_f32 v38, v36, v37
	ds_write_b64 v100, v[38:39] offset:28672
	s_add_u32 s0, s22, 0xe0e00
	s_addc_u32 s1, s90, 0
	s_add_u32 s100, s22, 0xe0e00
	s_addc_u32 s101, s90, 0
	global_load_dwordx4 v[36:39], v201, s[100:101] nt
	s_setprio 1
	s_waitcnt lgkmcnt(1)
	v_mfma_f32_16x16x32_f16 v[76:79], v[178:181], v[206:209], v[76:79]
	v_mfma_f32_16x16x32_f16 v[234:237], v[178:181], v[210:213], v[234:237]
	v_mfma_f32_16x16x32_f16 v[158:161], v[178:181], v[214:217], v[158:161]
	v_mfma_f32_16x16x32_f16 v[166:169], v[178:181], v[218:221], v[166:169]
	v_mfma_f32_16x16x32_f16 v[178:181], v[238:241], v[206:209], v[182:185]
	v_mfma_f32_16x16x32_f16 v[182:185], v[238:241], v[210:213], v[190:193]
	v_mfma_f32_16x16x32_f16 v[190:193], v[238:241], v[214:217], v[202:205]
	v_mfma_f32_16x16x32_f16 v[186:189], v[238:241], v[218:221], v[186:189]
	s_setprio 0
	s_waitcnt vmcnt(6)
	s_waitcnt lgkmcnt(0)
	s_barrier
	ds_read_b128 v[202:205], v131
	ds_read_b128 v[206:209], v131 offset:2048
	ds_read_b128 v[210:213], v131 offset:4096
	ds_read_b128 v[214:217], v131 offset:6144
	ds_read_b128 v[218:221], v129
	ds_read_b128 v[238:241], v129 offset:2048
	s_add_u32 s70, s22, 0xf00
	v_lshl_add_u64 v[92:93], s[52:53], 0, v[196:197]
	s_addc_u32 s71, s90, 0
	v_readfirstlane_b32 s0, v95
	s_mov_b32 m0, s0
	v_cvt_pk_f16_f32 v3, v2, v3
	global_load_lds_dwordx4 v[92:93], off
	v_cvt_pk_f16_f32 v2, v0, v1
	ds_write_b64 v100, v[2:3] offset:32768
	s_setprio 1
	s_waitcnt lgkmcnt(1)
	v_mfma_f32_16x16x32_f16 v[80:83], v[218:221], v[202:205], v[80:83]
	v_mfma_f32_16x16x32_f16 v[104:107], v[218:221], v[210:213], v[104:107]
	v_mfma_f32_16x16x32_f16 v[108:111], v[238:241], v[202:205], v[108:111]
	v_mfma_f32_16x16x32_f16 v[112:115], v[238:241], v[206:209], v[112:115]
	v_mfma_f32_16x16x32_f16 v[116:119], v[238:241], v[210:213], v[116:119]
	v_mfma_f32_16x16x32_f16 v[230:233], v[218:221], v[206:209], v[230:233]
	v_mfma_f32_16x16x32_f16 v[218:221], v[218:221], v[214:217], v[222:225]
	v_mfma_f32_16x16x32_f16 v[222:225], v[238:241], v[214:217], v[226:229]
	s_setprio 0
	s_nop 1
	ds_read_b128 v[226:229], v129 offset:4096
	ds_read_b128 v[238:241], v129 offset:6144
	v_readfirstlane_b32 s1, v96
	v_lshl_add_u64 v[198:199], v[92:93], 0, s[58:59]
	s_mov_b32 m0, s1
	v_cvt_pk_f16_f32 v7, v6, v7
	global_load_lds_dwordx4 v[198:199], off
	v_cvt_pk_f16_f32 v6, v4, v5
	ds_write_b64 v100, v[6:7] offset:36864
	s_add_u32 s70, s22, 0x20f00
	s_addc_u32 s71, s90, 0
	s_add_u32 s100, s22, 0xf00
	s_addc_u32 s101, s90, 0
	global_load_dwordx4 v[0:3], v201, s[100:101] nt
	s_setprio 1
	s_waitcnt lgkmcnt(1)
	v_mfma_f32_16x16x32_f16 v[68:71], v[226:229], v[202:205], v[68:71]
	v_mfma_f32_16x16x32_f16 v[64:67], v[226:229], v[206:209], v[64:67]
	v_mfma_f32_16x16x32_f16 v[84:87], v[226:229], v[210:213], v[84:87]
	v_mfma_f32_16x16x32_f16 v[120:123], v[226:229], v[214:217], v[120:123]
	v_mfma_f32_16x16x32_f16 v[124:127], v[238:241], v[202:205], v[124:127]
	v_mfma_f32_16x16x32_f16 v[134:137], v[238:241], v[214:217], v[134:137]
	v_mfma_f32_16x16x32_f16 v[138:141], v[238:241], v[206:209], v[138:141]
	v_mfma_f32_16x16x32_f16 v[142:145], v[238:241], v[210:213], v[142:145]
	s_setprio 0
	ds_read_b128 v[226:229], v129 offset:8192
	ds_read_b128 v[238:241], v129 offset:10240
	v_readfirstlane_b32 s70, v97
	v_lshl_add_u64 v[198:199], v[92:93], 0, s[60:61]
	s_mov_b32 m0, s70
	v_cvt_pk_f16_f32 v15, v14, v15
	global_load_lds_dwordx4 v[198:199], off
	v_cvt_pk_f16_f32 v14, v12, v13
	ds_write_b64 v100, v[14:15] offset:40960
	s_add_u32 s72, s22, 0x40f00
	s_addc_u32 s73, s90, 0
	s_add_u32 s100, s22, 0x20f00
	s_addc_u32 s101, s90, 0
	global_load_dwordx4 v[4:7], v201, s[100:101] nt
	s_setprio 1
	s_waitcnt lgkmcnt(1)
	v_mfma_f32_16x16x32_f16 v[72:75], v[226:229], v[202:205], v[72:75]
	v_mfma_f32_16x16x32_f16 v[88:91], v[226:229], v[206:209], v[88:91]
	v_mfma_f32_16x16x32_f16 v[146:149], v[226:229], v[214:217], v[146:149]
	v_mfma_f32_16x16x32_f16 v[170:173], v[226:229], v[210:213], v[170:173]
	v_mfma_f32_16x16x32_f16 v[150:153], v[238:241], v[202:205], v[150:153]
	v_mfma_f32_16x16x32_f16 v[162:165], v[238:241], v[206:209], v[162:165]
	v_mfma_f32_16x16x32_f16 v[174:177], v[238:241], v[210:213], v[174:177]
	v_mfma_f32_16x16x32_f16 v[154:157], v[238:241], v[214:217], v[154:157]
	s_setprio 0
	ds_read_b128 v[226:229], v129 offset:12288
	ds_read_b128 v[238:241], v129 offset:14336
	v_readfirstlane_b32 s71, v98
	v_lshl_add_u64 v[92:93], v[92:93], 0, s[62:63]
	s_mov_b32 m0, s71
	v_cvt_pk_f16_f32 v19, v18, v19
	global_load_lds_dwordx4 v[92:93], off
	v_cvt_pk_f16_f32 v18, v16, v17
	ds_write_b64 v100, v[18:19] offset:45056
	s_add_u32 s72, s22, 0x60f00
	s_addc_u32 s73, s90, 0
	s_add_u32 s100, s22, 0x40f00
	s_addc_u32 s101, s90, 0
	global_load_dwordx4 v[12:15], v201, s[100:101] nt
	s_setprio 1
	s_waitcnt lgkmcnt(1)
	v_mfma_f32_16x16x32_f16 v[76:79], v[226:229], v[202:205], v[76:79]
	v_mfma_f32_16x16x32_f16 v[234:237], v[226:229], v[206:209], v[234:237]
	v_mfma_f32_16x16x32_f16 v[158:161], v[226:229], v[210:213], v[158:161]
	v_mfma_f32_16x16x32_f16 v[166:169], v[226:229], v[214:217], v[166:169]
	v_mfma_f32_16x16x32_f16 v[178:181], v[238:241], v[202:205], v[178:181]
	v_mfma_f32_16x16x32_f16 v[182:185], v[238:241], v[206:209], v[182:185]
	v_mfma_f32_16x16x32_f16 v[190:193], v[238:241], v[210:213], v[190:193]
	v_mfma_f32_16x16x32_f16 v[186:189], v[238:241], v[214:217], v[186:189]
	s_setprio 0
	ds_read_b128 v[202:205], v128
	ds_read_b128 v[206:209], v128 offset:2048
	ds_read_b128 v[210:213], v128 offset:4096
	ds_read_b128 v[214:217], v128 offset:6144
	ds_read_b128 v[226:229], v130
	ds_read_b128 v[238:241], v130 offset:2048
	v_cvt_pk_f16_f32 v23, v22, v23
	v_cvt_pk_f16_f32 v22, v20, v21
	ds_write_b64 v100, v[22:23] offset:49152
	s_add_u32 s72, s22, 0x80f00
	s_addc_u32 s73, s90, 0
	s_add_u32 s100, s22, 0x60f00
	s_addc_u32 s101, s90, 0
	global_load_dwordx4 v[16:19], v201, s[100:101] nt
	s_add_u32 s100, s22, 0x80f00
	s_addc_u32 s101, s90, 0
	global_load_dwordx4 v[20:23], v201, s[100:101] nt
	s_setprio 1
	s_waitcnt lgkmcnt(1)
	v_mfma_f32_16x16x32_f16 v[80:83], v[226:229], v[202:205], v[80:83]
	v_mfma_f32_16x16x32_f16 v[104:107], v[226:229], v[210:213], v[104:107]
	v_mfma_f32_16x16x32_f16 v[108:111], v[238:241], v[202:205], v[108:111]
	v_mfma_f32_16x16x32_f16 v[112:115], v[238:241], v[206:209], v[112:115]
	v_mfma_f32_16x16x32_f16 v[116:119], v[238:241], v[210:213], v[116:119]
	v_mfma_f32_16x16x32_f16 v[230:233], v[226:229], v[206:209], v[230:233]
	v_mfma_f32_16x16x32_f16 v[218:221], v[226:229], v[214:217], v[218:221]
	v_mfma_f32_16x16x32_f16 v[222:225], v[238:241], v[214:217], v[222:225]
	s_setprio 0
	ds_read_b128 v[226:229], v130 offset:4096
	ds_read_b128 v[238:241], v130 offset:6144
	v_cvt_pk_f16_f32 v27, v26, v27
	v_cvt_pk_f16_f32 v26, v24, v25
	ds_write_b64 v100, v[26:27] offset:53248
	s_add_u32 s72, s22, 0xa0f00
	s_addc_u32 s73, s90, 0
	s_add_u32 s100, s22, 0xa0f00
	s_addc_u32 s101, s90, 0
	global_load_dwordx4 v[24:27], v201, s[100:101] nt
	s_setprio 1
	s_waitcnt lgkmcnt(1)
	v_mfma_f32_16x16x32_f16 v[68:71], v[226:229], v[202:205], v[68:71]
	v_mfma_f32_16x16x32_f16 v[64:67], v[226:229], v[206:209], v[64:67]
	v_mfma_f32_16x16x32_f16 v[84:87], v[226:229], v[210:213], v[84:87]
	v_mfma_f32_16x16x32_f16 v[120:123], v[226:229], v[214:217], v[120:123]
	v_mfma_f32_16x16x32_f16 v[124:127], v[238:241], v[202:205], v[124:127]
	v_mfma_f32_16x16x32_f16 v[134:137], v[238:241], v[214:217], v[134:137]
	v_mfma_f32_16x16x32_f16 v[138:141], v[238:241], v[206:209], v[138:141]
	v_mfma_f32_16x16x32_f16 v[142:145], v[238:241], v[210:213], v[142:145]
	s_setprio 0
	ds_read_b128 v[226:229], v130 offset:8192
	ds_read_b128 v[238:241], v130 offset:10240
	v_cvt_pk_f16_f32 v31, v30, v31
	v_cvt_pk_f16_f32 v30, v28, v29
	ds_write_b64 v100, v[30:31] offset:57344
	s_add_u32 s72, s22, 0xc0f00
	s_addc_u32 s73, s90, 0
	s_add_u32 s100, s22, 0xc0f00
	s_addc_u32 s101, s90, 0
	global_load_dwordx4 v[28:31], v201, s[100:101] nt
	s_setprio 1
	s_waitcnt lgkmcnt(1)
	v_mfma_f32_16x16x32_f16 v[72:75], v[226:229], v[202:205], v[72:75]
	v_mfma_f32_16x16x32_f16 v[88:91], v[226:229], v[206:209], v[88:91]
	v_mfma_f32_16x16x32_f16 v[146:149], v[226:229], v[214:217], v[146:149]
	v_mfma_f32_16x16x32_f16 v[170:173], v[226:229], v[210:213], v[170:173]
	v_mfma_f32_16x16x32_f16 v[150:153], v[238:241], v[202:205], v[150:153]
	v_mfma_f32_16x16x32_f16 v[162:165], v[238:241], v[206:209], v[162:165]
	v_mfma_f32_16x16x32_f16 v[174:177], v[238:241], v[210:213], v[174:177]
	v_mfma_f32_16x16x32_f16 v[154:157], v[238:241], v[214:217], v[154:157]
	s_setprio 0
	ds_read_b128 v[226:229], v130 offset:12288
	ds_read_b128 v[238:241], v130 offset:14336
	v_cvt_pk_f16_f32 v35, v34, v35
	v_cvt_pk_f16_f32 v34, v32, v33
	ds_write_b64 v100, v[34:35] offset:61440
	s_add_u32 s72, s22, 0xe0f00
	s_addc_u32 s73, s90, 0
	s_add_u32 s100, s22, 0xe0f00
	s_addc_u32 s101, s90, 0
	global_load_dwordx4 v[32:35], v201, s[100:101] nt
	s_setprio 1
	s_waitcnt lgkmcnt(1)
	v_mfma_f32_16x16x32_f16 v[76:79], v[226:229], v[202:205], v[76:79]
	v_mfma_f32_16x16x32_f16 v[234:237], v[226:229], v[206:209], v[234:237]
	v_mfma_f32_16x16x32_f16 v[158:161], v[226:229], v[210:213], v[158:161]
	v_mfma_f32_16x16x32_f16 v[166:169], v[226:229], v[214:217], v[166:169]
	v_mfma_f32_16x16x32_f16 v[178:181], v[238:241], v[202:205], v[178:181]
	v_mfma_f32_16x16x32_f16 v[182:185], v[238:241], v[206:209], v[182:185]
	v_mfma_f32_16x16x32_f16 v[190:193], v[238:241], v[210:213], v[190:193]
	v_mfma_f32_16x16x32_f16 v[186:189], v[238:241], v[214:217], v[186:189]
	s_setprio 0
	s_waitcnt vmcnt(6)
	s_waitcnt lgkmcnt(0)
	s_barrier
	ds_read_b128 v[202:205], v131 offset:32768
	ds_read_b128 v[206:209], v131 offset:34816
	ds_read_b128 v[210:213], v131 offset:36864
	ds_read_b128 v[214:217], v131 offset:38912
	ds_read_b128 v[226:229], v129 offset:32768
	ds_read_b128 v[238:241], v129 offset:34816
	v_lshl_add_u64 v[198:199], s[54:55], 0, v[196:197]
	v_readfirstlane_b32 s64, v94
	s_mov_b32 m0, s64
	v_cvt_pk_f16_f32 v11, v10, v11
	global_load_lds_dwordx4 v[198:199], off
	v_cvt_pk_f16_f32 v10, v8, v9
	ds_write_b64 v100, v[10:11]
	s_setprio 1
	s_waitcnt lgkmcnt(1)
	v_mfma_f32_16x16x32_f16 v[8:11], v[226:229], v[202:205], v[80:83]
	v_mfma_f32_16x16x32_f16 v[80:83], v[226:229], v[206:209], v[230:233]
	v_mfma_f32_16x16x32_f16 v[92:95], v[226:229], v[210:213], v[104:107]
	v_mfma_f32_16x16x32_f16 v[104:107], v[226:229], v[214:217], v[218:221]
	v_mfma_f32_16x16x32_f16 v[108:111], v[238:241], v[202:205], v[108:111]
	v_mfma_f32_16x16x32_f16 v[112:115], v[238:241], v[206:209], v[112:115]
	v_mfma_f32_16x16x32_f16 v[116:119], v[238:241], v[210:213], v[116:119]
	v_mfma_f32_16x16x32_f16 v[218:221], v[238:241], v[214:217], v[222:225]
	s_setprio 0
	s_nop 1
	ds_read_b128 v[222:225], v129 offset:36864
	ds_read_b128 v[226:229], v129 offset:38912
	v_readfirstlane_b32 s64, v99
	v_lshl_add_u64 v[96:97], v[198:199], 0, s[58:59]
	s_mov_b32 m0, s64
	v_cvt_pk_f16_f32 v43, v42, v43
	global_load_lds_dwordx4 v[96:97], off
	v_cvt_pk_f16_f32 v42, v40, v41
	ds_write_b64 v100, v[42:43] offset:4096
	s_setprio 1
	s_waitcnt lgkmcnt(1)
	v_mfma_f32_16x16x32_f16 v[40:43], v[222:225], v[202:205], v[68:71]
	v_mfma_f32_16x16x32_f16 v[64:67], v[222:225], v[206:209], v[64:67]
	v_mfma_f32_16x16x32_f16 v[68:71], v[222:225], v[210:213], v[84:87]
	v_mfma_f32_16x16x32_f16 v[84:87], v[222:225], v[214:217], v[120:123]
	v_mfma_f32_16x16x32_f16 v[96:99], v[226:229], v[202:205], v[124:127]
	v_mfma_f32_16x16x32_f16 v[120:123], v[226:229], v[206:209], v[138:141]
	v_mfma_f32_16x16x32_f16 v[124:127], v[226:229], v[210:213], v[142:145]
	v_mfma_f32_16x16x32_f16 v[134:137], v[226:229], v[214:217], v[134:137]
	s_setprio 0
	ds_read_b128 v[138:141], v129 offset:40960
	ds_read_b128 v[142:145], v129 offset:43008
	v_readfirstlane_b32 s64, v101
	v_lshl_add_u64 v[222:223], v[198:199], 0, s[60:61]
	s_mov_b32 m0, s64
	v_cvt_pk_f16_f32 v47, v46, v47
	global_load_lds_dwordx4 v[222:223], off
	v_cvt_pk_f16_f32 v46, v44, v45
	ds_write_b64 v100, v[46:47] offset:8192
	s_setprio 1
	s_waitcnt lgkmcnt(1)
	v_mfma_f32_16x16x32_f16 v[44:47], v[138:141], v[202:205], v[72:75]
	v_mfma_f32_16x16x32_f16 v[72:75], v[138:141], v[206:209], v[88:91]
	v_mfma_f32_16x16x32_f16 v[88:91], v[138:141], v[210:213], v[170:173]
	v_mfma_f32_16x16x32_f16 v[138:141], v[138:141], v[214:217], v[146:149]
	v_mfma_f32_16x16x32_f16 v[146:149], v[142:145], v[202:205], v[150:153]
	v_mfma_f32_16x16x32_f16 v[150:153], v[142:145], v[206:209], v[162:165]
	v_mfma_f32_16x16x32_f16 v[162:165], v[142:145], v[210:213], v[174:177]
	v_mfma_f32_16x16x32_f16 v[142:145], v[142:145], v[214:217], v[154:157]
	s_setprio 0
	s_nop 1
	ds_read_b128 v[154:157], v129 offset:45056
	ds_read_b128 v[170:173], v129 offset:47104
	v_readfirstlane_b32 s64, v102
	v_lshl_add_u64 v[174:175], v[198:199], 0, s[62:63]
	s_mov_b32 m0, s64
	v_cvt_pk_f16_f32 v51, v50, v51
	global_load_lds_dwordx4 v[174:175], off
	v_cvt_pk_f16_f32 v50, v48, v49
	ds_write_b64 v100, v[50:51] offset:12288
	s_setprio 1
	s_waitcnt lgkmcnt(1)
	v_mfma_f32_16x16x32_f16 v[48:51], v[154:157], v[202:205], v[76:79]
	v_mfma_f32_16x16x32_f16 v[76:79], v[154:157], v[206:209], v[234:237]
	v_mfma_f32_16x16x32_f16 v[158:161], v[154:157], v[210:213], v[158:161]
	v_mfma_f32_16x16x32_f16 v[154:157], v[154:157], v[214:217], v[166:169]
	v_mfma_f32_16x16x32_f16 v[166:169], v[170:173], v[202:205], v[178:181]
	v_mfma_f32_16x16x32_f16 v[174:177], v[170:173], v[206:209], v[182:185]
	v_mfma_f32_16x16x32_f16 v[178:181], v[170:173], v[210:213], v[190:193]
	v_mfma_f32_16x16x32_f16 v[170:173], v[170:173], v[214:217], v[186:189]
	s_setprio 0
	ds_read_b128 v[182:185], v128 offset:32768
	s_nop 0
	ds_read_b128 v[186:189], v128 offset:34816
	ds_read_b128 v[190:193], v128 offset:36864
	ds_read_b128 v[202:205], v128 offset:38912
	ds_read_b128 v[206:209], v130 offset:32768
	ds_read_b128 v[210:213], v130 offset:34816
	v_cvt_pk_f16_f32 v55, v54, v55
	v_cvt_pk_f16_f32 v54, v52, v53
	ds_write_b64 v100, v[54:55] offset:16384
	s_setprio 1
	s_waitcnt lgkmcnt(1)
	v_mfma_f32_16x16x32_f16 v[8:11], v[206:209], v[182:185], v[8:11]
	v_mfma_f32_16x16x32_f16 v[52:55], v[206:209], v[186:189], v[80:83]
	v_mfma_f32_16x16x32_f16 v[80:83], v[206:209], v[190:193], v[92:95]
	v_mfma_f32_16x16x32_f16 v[92:95], v[206:209], v[202:205], v[104:107]
	v_mfma_f32_16x16x32_f16 v[102:105], v[210:213], v[182:185], v[108:111]
	v_mfma_f32_16x16x32_f16 v[106:109], v[210:213], v[186:189], v[112:115]
	v_mfma_f32_16x16x32_f16 v[110:113], v[210:213], v[190:193], v[116:119]
	v_mfma_f32_16x16x32_f16 v[114:117], v[210:213], v[202:205], v[218:221]
	s_setprio 0
	ds_read_b128 v[206:209], v130 offset:36864
	ds_read_b128 v[210:213], v130 offset:38912
	v_cvt_pk_f16_f32 v59, v58, v59
	v_cvt_pk_f16_f32 v58, v56, v57
	ds_write_b64 v100, v[58:59] offset:20480
	s_setprio 1
	s_waitcnt lgkmcnt(1)
	v_mfma_f32_16x16x32_f16 v[40:43], v[206:209], v[182:185], v[40:43]
	v_mfma_f32_16x16x32_f16 v[56:59], v[206:209], v[186:189], v[64:67]
	v_mfma_f32_16x16x32_f16 v[64:67], v[206:209], v[190:193], v[68:71]
	v_mfma_f32_16x16x32_f16 v[68:71], v[206:209], v[202:205], v[84:87]
	v_mfma_f32_16x16x32_f16 v[84:87], v[210:213], v[182:185], v[96:99]
	v_mfma_f32_16x16x32_f16 v[96:99], v[210:213], v[186:189], v[120:123]
	v_mfma_f32_16x16x32_f16 v[118:121], v[210:213], v[190:193], v[124:127]
	v_mfma_f32_16x16x32_f16 v[122:125], v[210:213], v[202:205], v[134:137]
	s_setprio 0
	s_nop 1
	ds_read_b128 v[134:137], v130 offset:40960
	ds_read_b128 v[206:209], v130 offset:43008
	v_cvt_pk_f16_f32 v63, v62, v63
	v_cvt_pk_f16_f32 v62, v60, v61
	ds_write_b64 v100, v[62:63] offset:24576
	s_setprio 1
	s_waitcnt lgkmcnt(1)
	v_mfma_f32_16x16x32_f16 v[44:47], v[134:137], v[182:185], v[44:47]
	v_mfma_f32_16x16x32_f16 v[60:63], v[134:137], v[186:189], v[72:75]
	v_mfma_f32_16x16x32_f16 v[72:75], v[134:137], v[190:193], v[88:91]
	v_mfma_f32_16x16x32_f16 v[88:91], v[134:137], v[202:205], v[138:141]
	v_mfma_f32_16x16x32_f16 v[134:137], v[206:209], v[182:185], v[146:149]
	v_mfma_f32_16x16x32_f16 v[146:149], v[206:209], v[190:193], v[162:165]
	v_mfma_f32_16x16x32_f16 v[138:141], v[206:209], v[186:189], v[150:153]
	v_mfma_f32_16x16x32_f16 v[142:145], v[206:209], v[202:205], v[142:145]
	s_setprio 0
	s_nop 0
	ds_read_b128 v[150:153], v130 offset:45056
	ds_read_b128 v[162:165], v130 offset:47104
	v_cvt_pk_f16_f32 v39, v38, v39
	v_cvt_pk_f16_f32 v38, v36, v37
	ds_write_b64 v100, v[38:39] offset:28672
	s_setprio 1
	s_waitcnt lgkmcnt(1)
	v_mfma_f32_16x16x32_f16 v[36:39], v[150:153], v[182:185], v[48:51]
	v_mfma_f32_16x16x32_f16 v[48:51], v[150:153], v[186:189], v[76:79]
	v_mfma_f32_16x16x32_f16 v[76:79], v[150:153], v[190:193], v[158:161]
	v_mfma_f32_16x16x32_f16 v[150:153], v[150:153], v[202:205], v[154:157]
	v_mfma_f32_16x16x32_f16 v[154:157], v[162:165], v[182:185], v[166:169]
	v_mfma_f32_16x16x32_f16 v[158:161], v[162:165], v[186:189], v[174:177]
	v_mfma_f32_16x16x32_f16 v[166:169], v[162:165], v[190:193], v[178:181]
	v_mfma_f32_16x16x32_f16 v[162:165], v[162:165], v[202:205], v[170:173]
	s_setprio 0
	s_waitcnt vmcnt(0)
	s_waitcnt lgkmcnt(0)
	s_barrier
	s_nop 0
	ds_read_b128 v[170:173], v131
	ds_read_b128 v[174:177], v131 offset:2048
	ds_read_b128 v[178:181], v131 offset:4096
	ds_read_b128 v[182:185], v131 offset:6144
	ds_read_b128 v[186:189], v129
	ds_read_b128 v[190:193], v129 offset:2048
	v_lshl_add_u64 v[126:127], s[56:57], 0, v[196:197]
	s_mov_b32 m0, s0
	v_cvt_pk_f16_f32 v3, v2, v3
	global_load_lds_dwordx4 v[126:127], off
	v_cvt_pk_f16_f32 v2, v0, v1
	ds_write_b64 v100, v[2:3] offset:32768
	s_setprio 1
	s_waitcnt lgkmcnt(1)
	v_mfma_f32_16x16x32_f16 v[0:3], v[186:189], v[170:173], v[8:11]
	v_mfma_f32_16x16x32_f16 v[8:11], v[186:189], v[174:177], v[52:55]
	v_mfma_f32_16x16x32_f16 v[52:55], v[186:189], v[178:181], v[80:83]
	v_mfma_f32_16x16x32_f16 v[80:83], v[186:189], v[182:185], v[92:95]
	v_mfma_f32_16x16x32_f16 v[92:95], v[190:193], v[170:173], v[102:105]
	v_mfma_f32_16x16x32_f16 v[102:105], v[190:193], v[174:177], v[106:109]
	v_mfma_f32_16x16x32_f16 v[106:109], v[190:193], v[178:181], v[110:113]
	v_mfma_f32_16x16x32_f16 v[110:113], v[190:193], v[182:185], v[114:117]
	s_setprio 0
	s_nop 1
	ds_read_b128 v[114:117], v129 offset:4096
	ds_read_b128 v[186:189], v129 offset:6144
	s_mov_b32 m0, s1
	v_lshl_add_u64 v[190:191], v[126:127], 0, s[58:59]
	global_load_lds_dwordx4 v[190:191], off
	v_cvt_pk_f16_f32 v7, v6, v7
	v_cvt_pk_f16_f32 v6, v4, v5
	ds_write_b64 v100, v[6:7] offset:36864
	s_setprio 1
	s_waitcnt lgkmcnt(1)
	v_mfma_f32_16x16x32_f16 v[190:193], v[114:117], v[170:173], v[40:43]
	v_mfma_f32_16x16x32_f16 v[56:59], v[114:117], v[174:177], v[56:59]
	v_mfma_f32_16x16x32_f16 v[64:67], v[114:117], v[178:181], v[64:67]
	v_mfma_f32_16x16x32_f16 v[68:71], v[114:117], v[182:185], v[68:71]
	v_mfma_f32_16x16x32_f16 v[84:87], v[186:189], v[170:173], v[84:87]
	v_mfma_f32_16x16x32_f16 v[96:99], v[186:189], v[174:177], v[96:99]
	v_mfma_f32_16x16x32_f16 v[114:117], v[186:189], v[178:181], v[118:121]
	v_mfma_f32_16x16x32_f16 v[118:121], v[186:189], v[182:185], v[122:125]
	s_setprio 0
	ds_read_b128 v[4:7], v129 offset:8192
	ds_read_b128 v[40:43], v129 offset:10240
	s_mov_b32 m0, s70
	v_lshl_add_u64 v[122:123], v[126:127], 0, s[60:61]
	global_load_lds_dwordx4 v[122:123], off
	v_cvt_pk_f16_f32 v15, v14, v15
	v_cvt_pk_f16_f32 v14, v12, v13
	ds_write_b64 v100, v[14:15] offset:40960
	s_setprio 1
	s_waitcnt lgkmcnt(1)
	v_mfma_f32_16x16x32_f16 v[122:125], v[4:7], v[170:173], v[44:47]
	v_mfma_f32_16x16x32_f16 v[88:91], v[4:7], v[182:185], v[88:91]
	v_mfma_f32_16x16x32_f16 v[134:137], v[40:43], v[170:173], v[134:137]
	v_mfma_f32_16x16x32_f16 v[146:149], v[40:43], v[178:181], v[146:149]
	v_mfma_f32_16x16x32_f16 v[186:189], v[4:7], v[174:177], v[60:63]
	v_mfma_f32_16x16x32_f16 v[202:205], v[4:7], v[178:181], v[72:75]
	v_mfma_f32_16x16x32_f16 v[138:141], v[40:43], v[174:177], v[138:141]
	v_mfma_f32_16x16x32_f16 v[142:145], v[40:43], v[182:185], v[142:145]
	s_setprio 0
	ds_read_b128 v[4:7], v129 offset:12288
	ds_read_b128 v[12:15], v129 offset:14336
	s_mov_b32 m0, s71
	v_lshl_add_u64 v[40:41], v[126:127], 0, s[62:63]
	global_load_lds_dwordx4 v[40:41], off
	v_cvt_pk_f16_f32 v19, v18, v19
	v_cvt_pk_f16_f32 v18, v16, v17
	ds_write_b64 v100, v[18:19] offset:45056
	s_setprio 1
	s_waitcnt lgkmcnt(1)
	v_mfma_f32_16x16x32_f16 v[206:209], v[4:7], v[170:173], v[36:39]
	v_mfma_f32_16x16x32_f16 v[210:213], v[4:7], v[174:177], v[48:51]
	v_mfma_f32_16x16x32_f16 v[214:217], v[4:7], v[178:181], v[76:79]
	v_mfma_f32_16x16x32_f16 v[150:153], v[4:7], v[182:185], v[150:153]
	v_mfma_f32_16x16x32_f16 v[154:157], v[12:15], v[170:173], v[154:157]
	v_mfma_f32_16x16x32_f16 v[158:161], v[12:15], v[174:177], v[158:161]
	v_mfma_f32_16x16x32_f16 v[166:169], v[12:15], v[178:181], v[166:169]
	v_mfma_f32_16x16x32_f16 v[162:165], v[12:15], v[182:185], v[162:165]
	s_setprio 0
	ds_read_b128 v[170:173], v128
	ds_read_b128 v[174:177], v128 offset:2048
	ds_read_b128 v[178:181], v128 offset:4096
	ds_read_b128 v[182:185], v128 offset:6144
	ds_read_b128 v[12:15], v130
	ds_read_b128 v[40:43], v130 offset:2048
	v_cvt_pk_f16_f32 v5, v22, v23
	v_cvt_pk_f16_f32 v4, v20, v21
	ds_write_b64 v100, v[4:5] offset:49152
	s_setprio 1
	s_waitcnt lgkmcnt(1)
	v_mfma_f32_16x16x32_f16 v[0:3], v[12:15], v[170:173], v[0:3]
	v_mfma_f32_16x16x32_f16 v[4:7], v[12:15], v[174:177], v[8:11]
	v_mfma_f32_16x16x32_f16 v[8:11], v[12:15], v[178:181], v[52:55]
	v_mfma_f32_16x16x32_f16 v[12:15], v[12:15], v[182:185], v[80:83]
	v_mfma_f32_16x16x32_f16 v[16:19], v[40:43], v[170:173], v[92:95]
	v_mfma_f32_16x16x32_f16 v[20:23], v[40:43], v[174:177], v[102:105]
	v_mfma_f32_16x16x32_f16 v[36:39], v[40:43], v[178:181], v[106:109]
	v_mfma_f32_16x16x32_f16 v[40:43], v[40:43], v[182:185], v[110:113]
	s_setprio 0
	ds_read_b128 v[52:55], v130 offset:4096
	ds_read_b128 v[72:75], v130 offset:6144
	v_cvt_pk_f16_f32 v27, v26, v27
	v_cvt_pk_f16_f32 v26, v24, v25
	ds_write_b64 v100, v[26:27] offset:53248
	s_setprio 1
	s_waitcnt lgkmcnt(1)
	v_mfma_f32_16x16x32_f16 v[24:27], v[52:55], v[170:173], v[190:193]
	v_mfma_f32_16x16x32_f16 v[44:47], v[52:55], v[174:177], v[56:59]
	v_mfma_f32_16x16x32_f16 v[48:51], v[52:55], v[178:181], v[64:67]
	v_mfma_f32_16x16x32_f16 v[52:55], v[52:55], v[182:185], v[68:71]
	v_mfma_f32_16x16x32_f16 v[56:59], v[72:75], v[170:173], v[84:87]
	v_mfma_f32_16x16x32_f16 v[60:63], v[72:75], v[174:177], v[96:99]
	v_mfma_f32_16x16x32_f16 v[64:67], v[72:75], v[178:181], v[114:117]
	v_mfma_f32_16x16x32_f16 v[68:71], v[72:75], v[182:185], v[118:121]
	s_setprio 0
	ds_read_b128 v[80:83], v130 offset:8192
	ds_read_b128 v[96:99], v130 offset:10240
	v_cvt_pk_f16_f32 v31, v30, v31
	v_cvt_pk_f16_f32 v30, v28, v29
	ds_write_b64 v100, v[30:31] offset:57344
	s_setprio 1
	s_waitcnt lgkmcnt(1)
	v_mfma_f32_16x16x32_f16 v[28:31], v[80:83], v[170:173], v[122:125]
	v_mfma_f32_16x16x32_f16 v[72:75], v[80:83], v[174:177], v[186:189]
	v_mfma_f32_16x16x32_f16 v[76:79], v[80:83], v[178:181], v[202:205]
	v_mfma_f32_16x16x32_f16 v[80:83], v[80:83], v[182:185], v[88:91]
	v_mfma_f32_16x16x32_f16 v[84:87], v[96:99], v[170:173], v[134:137]
	v_mfma_f32_16x16x32_f16 v[88:91], v[96:99], v[174:177], v[138:141]
	v_mfma_f32_16x16x32_f16 v[92:95], v[96:99], v[178:181], v[146:149]
	v_mfma_f32_16x16x32_f16 v[96:99], v[96:99], v[182:185], v[142:145]
	s_setprio 0
	ds_read_b128 v[108:111], v130 offset:12288
	ds_read_b128 v[124:127], v130 offset:14336
	v_cvt_pk_f16_f32 v35, v34, v35
	v_cvt_pk_f16_f32 v34, v32, v33
	ds_write_b64 v100, v[34:35] offset:61440
	s_setprio 1
	s_waitcnt lgkmcnt(1)
	v_mfma_f32_16x16x32_f16 v[32:35], v[108:111], v[170:173], v[206:209]
	v_mfma_f32_16x16x32_f16 v[100:103], v[108:111], v[174:177], v[210:213]
	v_mfma_f32_16x16x32_f16 v[104:107], v[108:111], v[178:181], v[214:217]
	v_mfma_f32_16x16x32_f16 v[108:111], v[108:111], v[182:185], v[150:153]
	v_mfma_f32_16x16x32_f16 v[112:115], v[124:127], v[170:173], v[154:157]
	v_mfma_f32_16x16x32_f16 v[116:119], v[124:127], v[174:177], v[158:161]
	v_mfma_f32_16x16x32_f16 v[120:123], v[124:127], v[178:181], v[166:169]
	v_mfma_f32_16x16x32_f16 v[124:127], v[124:127], v[182:185], v[162:165]
	s_setprio 0
	s_waitcnt vmcnt(0)
	s_waitcnt lgkmcnt(0)
	s_barrier
	ds_read_b128 v[134:137], v131 offset:32768
	ds_read_b128 v[138:141], v131 offset:34816
	ds_read_b128 v[142:145], v131 offset:36864
	ds_read_b128 v[148:151], v131 offset:38912
	ds_read_b128 v[152:155], v129 offset:32768
	ds_read_b128 v[156:159], v129 offset:34816
	s_setprio 1
	s_waitcnt lgkmcnt(0)
	v_mfma_f32_16x16x32_f16 v[0:3], v[152:155], v[134:137], v[0:3]
	v_mfma_f32_16x16x32_f16 v[4:7], v[152:155], v[138:141], v[4:7]
	v_mfma_f32_16x16x32_f16 v[8:11], v[152:155], v[142:145], v[8:11]
	v_mfma_f32_16x16x32_f16 v[12:15], v[152:155], v[148:151], v[12:15]
	v_mfma_f32_16x16x32_f16 v[16:19], v[156:159], v[134:137], v[16:19]
	v_mfma_f32_16x16x32_f16 v[20:23], v[156:159], v[138:141], v[20:23]
	v_mfma_f32_16x16x32_f16 v[36:39], v[156:159], v[142:145], v[36:39]
	v_mfma_f32_16x16x32_f16 v[40:43], v[156:159], v[148:151], v[40:43]
	s_setprio 0
	ds_read_b128 v[152:155], v129 offset:36864
	ds_read_b128 v[156:159], v129 offset:38912
	v_and_b32_e32 v250, 0x7ffffc00, v194
	v_lshl_add_u64 v[252:253], s[10:11], 0, v[196:197]
	v_readfirstlane_b32 s32, v250
	s_nop 0
	s_mov_b32 m0, s32
	s_nop 0
	global_load_lds_dwordx4 v[252:253], off
	v_mov_b32_e32 v146, 0
	v_and_b32_e32 v251, 0xfffffff, v132
	v_cmp_gt_u32_e32 vcc, s82, v251
	v_mov_b32_e32 v132, 0
	v_mov_b32_e32 v133, 0
	s_and_saveexec_b64 s[0:1], vcc
	s_cbranch_execz .LBB1_7
	s_and_b32 s64, s78, 0x7ffffc00
	s_or_b32 s64, s64, s33
	v_or_b32_e32 v132, s64, v251
	v_mov_b32_e32 v133, v195
	v_lshl_add_u64 v[132:133], v[132:133], 2, s[12:13]
	global_load_dword v133, v[132:133], off
	v_or_b32_e32 v132, s33, v251
	v_lshlrev_b32_e32 v132, 2, v132
	global_load_dword v146, v132, s[16:17]
	s_nop 0
	global_load_dword v132, v132, s[14:15]
